# v037 + xor-16 / xor-32 reduction steps via v_permlane16/32_swap instead of ds_swizzle / ds_bpermute round trips
# baseline (speedup 1.0000x reference)
; __device__ __forceinline__ unsigned pk2(float lo, float hi) { unsigned r; asm("v_cvt_pk_bf16_f32 %0, %1, %2" : "=v"(r) : "v"(lo), "v"(hi)); return r; }
; __device__ __forceinline__ float bflo(unsigned w) { return __uint_as_float(w << 16); }
; __device__ __forceinline__ float bfhi(unsigned w) { return __uint_as_float(w & 0xffff0000u); }
; __device__ __forceinline__ float wave_sum(float v) {
;     v += SHX(v, 1); v += SHX(v, 2); v += SHX(v, 4); v += SHX(v, 8); v += SHX(v, 16); v += SHX(v, 32);
;     return v;
; template <int MODE>
; __device__ __forceinline__ void phase_rowpass1(const Ptrs& P, LAS unsigned char* lds, int layer, int tid_, int vcu, int G) {
;     ...
;             f32x4 e[4]; float ss = 0.f;
; #pragma unroll
;             for (int jp = 0; jp < 2; ++jp) { const v4u hw = ((const v4u*)(H + (size_t)row * D))[lane + 64 * jp]; const v4u w = __builtin_nontemporal_load((const v4u*)(GE + (size_t)row * D) + lane + 64 * jp);
;                 v[2 * jp] = (f32x4){bflo(hw.x), bfhi(hw.x), bflo(hw.y), bfhi(hw.y)}; v[2 * jp + 1] = (f32x4){bflo(hw.z), bfhi(hw.z), bflo(hw.w), bfhi(hw.w)};
;                 e[2 * jp] = (f32x4){bflo(w.x), bfhi(w.x), bflo(w.y), bfhi(w.y)}; e[2 * jp + 1] = (f32x4){bflo(w.z), bfhi(w.z), bflo(w.w), bfhi(w.w)}; }
; #pragma unroll
;             for (int j = 0; j < 4; ++j) ss += e[j][0] * e[j][0] + e[j][1] * e[j][1] + e[j][2] * e[j][2] + e[j][3] * e[j][3];
;             const float r = rsqrtf(wave_sum(ss) * (1.f / D) + EPS);
; #pragma unroll
;             for (int j = 0; j < 4; ++j) { const f32x4 g = ((const f32x4*)pg)[F4(j)]; v[j] = v[j] + e[j] * r * g; }
;         }
;         if (MODE != 2) {
; #pragma unroll
;             for (int jp = 0; jp < 2; ++jp) { v4u hw; hw.x = pk2(v[2 * jp][0], v[2 * jp][1]); hw.y = pk2(v[2 * jp][2], v[2 * jp][3]); hw.z = pk2(v[2 * jp + 1][0], v[2 * jp + 1][1]); hw.w = pk2(v[2 * jp + 1][2], v[2 * jp + 1][3]);
;                 ((v4u*)(H + (size_t)row * D))[lane + 64 * jp] = hw; }
;         }
;         float ss = 0.f;
; #pragma unroll
;         for (int j = 0; j < 4; ++j) ss += v[j][0] * v[j][0] + v[j][1] * v[j][1] + v[j][2] * v[j][2] + v[j][3] * v[j][3];
;         const float rstd = rsqrtf(wave_sum(ss) * (1.f / D) + EPS);
; #pragma unroll
;         for (int j = 0; j < 4; ++j) { const f32x4 g = ((const f32x4*)g1)[F4(j)]; v[j] = v[j] * rstd * g; }
.LBB0_266:
	v_lshl_add_u64 v[22:23], s[0:1], 0, v[20:21]
	v_add_co_u32_e32 v24, vcc, 0x34600000, v22
	s_nop 1
	v_addc_co_u32_e32 v25, vcc, 0, v23, vcc
	s_waitcnt vmcnt(2)
	v_lshlrev_b32_e32 v4, 16, v232
	v_and_b32_e32 v5, 0xffff0000, v232
	v_lshlrev_b32_e32 v8, 16, v233
	v_and_b32_e32 v9, 0xffff0000, v233
	s_waitcnt lgkmcnt(0)
	v_lshlrev_b32_e32 v2, 16, v234
	v_and_b32_e32 v3, 0xffff0000, v234
	v_lshlrev_b32_e32 v6, 16, v235
	v_and_b32_e32 v7, 0xffff0000, v235
	v_and_b32_e32 v37, 0xffff0000, v238
	v_and_b32_e32 v36, 0xffff0000, v236
	v_lshlrev_b32_e32 v35, 16, v238
	v_lshlrev_b32_e32 v34, 16, v236
	v_lshlrev_b32_e32 v52, 16, v237
	v_and_b32_e32 v54, 0xffff0000, v237
	v_pk_mul_f32 v[30:31], v[36:37], v[36:37]
	v_lshlrev_b32_e32 v53, 16, v239
	v_and_b32_e32 v55, 0xffff0000, v239
	v_pk_fma_f32 v[30:31], v[34:35], v[34:35], v[30:31]
	v_lshlrev_b32_e32 v46, 16, v240
	v_and_b32_e32 v45, 0xffff0000, v248
	v_and_b32_e32 v44, 0xffff0000, v250
	v_lshlrev_b32_e32 v43, 16, v248
	v_lshlrev_b32_e32 v42, 16, v250
	v_pk_mul_f32 v[32:33], v[44:45], v[44:45]
	v_pk_fma_f32 v[30:31], v[52:53], v[52:53], v[30:31]
	v_lshlrev_b32_e32 v39, 16, v249
	v_lshlrev_b32_e32 v38, 16, v251
	v_pk_fma_f32 v[32:33], v[42:43], v[42:43], v[32:33]
	v_pk_fma_f32 v[30:31], v[54:55], v[54:55], v[30:31]
	v_and_b32_e32 v41, 0xffff0000, v249
	v_and_b32_e32 v40, 0xffff0000, v251
	v_pk_fma_f32 v[32:33], v[38:39], v[38:39], v[32:33]
	v_add_f32_e32 v30, v30, v31
	v_pk_fma_f32 v[32:33], v[40:41], v[40:41], v[32:33]
	v_and_b32_e32 v47, 0xffff0000, v240
	v_add_f32_e32 v30, v30, v33
	v_add_f32_e32 v30, v32, v30
	v_lshlrev_b32_e32 v48, 16, v241
	v_and_b32_e32 v49, 0xffff0000, v241
	v_lshlrev_b32_e32 v26, 16, v242
	v_and_b32_e32 v27, 0xffff0000, v242
	s_waitcnt lgkmcnt(0)
	s_nop 1
	v_add_f32_dpp v30, v30, v30 quad_perm:[1,0,3,2] row_mask:0xf bank_mask:0xf
	v_lshlrev_b32_e32 v28, 16, v243
	v_and_b32_e32 v29, 0xffff0000, v243
	v_add_u32_e32 v160, s74, v10
	v_cmp_gt_i32_e32 vcc, 0x4000, v160
	v_lshl_add_u64 v[160:161], v[20:21], 0, s[94:95]
	s_nop 0
	v_cndmask_b32_e32 v160, v20, v160, vcc
	v_cndmask_b32_e32 v161, v21, v161, vcc
	v_lshl_add_u64 v[160:161], s[0:1], 0, v[160:161]
	v_add_co_u32_e32 v244, vcc, 0x34600000, v160
	s_nop 1
	v_addc_co_u32_e32 v245, vcc, 0, v161, vcc
	v_add_co_u32_e32 v160, vcc, 0x65a00000, v160
	s_nop 1
	v_addc_co_u32_e32 v161, vcc, 0, v161, vcc
	global_load_dwordx4 v[232:235], v[244:245], off
	global_load_dwordx4 v[236:239], v[160:161], off nt
	global_load_dwordx4 v[240:243], v[244:245], off offset:1024
	global_load_dwordx4 v[248:251], v[160:161], off offset:1024 nt
	s_waitcnt lgkmcnt(0)
	s_nop 1
	v_add_f32_dpp v30, v30, v30 quad_perm:[2,3,0,1] row_mask:0xf bank_mask:0xf
	s_waitcnt lgkmcnt(0)
	s_nop 1
	v_add_f32_dpp v30, v30, v30 row_half_mirror row_mask:0xf bank_mask:0xf
	s_waitcnt lgkmcnt(0)
	s_nop 1
	v_add_f32_dpp v30, v30, v30 row_mirror row_mask:0xf bank_mask:0xf
	v_mov_b32_e32 v31, v30
	s_nop 1
	v_permlane16_swap_b32 v30, v31
	s_waitcnt lgkmcnt(0)
	v_add_f32_e32 v30, v30, v31
	s_nop 0
	v_mov_b32_e32 v31, v30
	s_nop 1
	v_permlane32_swap_b32 v30, v31
	s_waitcnt lgkmcnt(0)
	v_add_f32_e32 v30, v30, v31
	v_fmamk_f32 v30, v30, 0x3a800000, v196
	v_cmp_gt_f32_e32 vcc, s73, v30
	v_mul_f32_e32 v31, 0x4b800000, v30
	s_nop 0
	v_cndmask_b32_e32 v30, v30, v31, vcc
	v_rsq_f32_e32 v30, v30
	s_nop 0
	v_mul_f32_e32 v31, 0x45800000, v30
	v_cndmask_b32_e32 v50, v30, v31, vcc
	v_mov_b32_e32 v30, v34
	v_mov_b32_e32 v31, v36
	v_pk_mul_f32 v[32:33], v[30:31], v[50:51] op_sel_hi:[1,0]
	v_mov_b32_e32 v30, v52
	v_mov_b32_e32 v31, v54
	v_pk_mul_f32 v[30:31], v[30:31], v[50:51] op_sel_hi:[1,0]
	v_mov_b32_e32 v36, v35
	v_mov_b32_e32 v54, v53
	v_mov_b32_e32 v52, v43
	v_mov_b32_e32 v43, v44
	v_mov_b32_e32 v53, v45
	v_pk_mul_f32 v[42:43], v[42:43], v[50:51] op_sel_hi:[1,0]
	v_pk_mul_f32 v[52:53], v[52:53], v[50:51] op_sel_hi:[1,0]
	v_pk_fma_f32 v[30:31], v[66:67], v[30:31], v[8:9]
	v_pk_fma_f32 v[32:33], v[64:65], v[32:33], v[4:5]
	v_pk_mul_f32 v[4:5], v[36:37], v[50:51] op_sel_hi:[1,0]
	v_pk_mul_f32 v[8:9], v[54:55], v[50:51] op_sel_hi:[1,0]
	v_pk_fma_f32 v[36:37], v[68:69], v[4:5], v[2:3]
	v_pk_fma_f32 v[34:35], v[70:71], v[8:9], v[6:7]
	v_mov_b32_e32 v54, v39
	v_mov_b32_e32 v55, v41
	v_mov_b32_e32 v39, v40
	v_pk_mul_f32 v[54:55], v[54:55], v[50:51] op_sel_hi:[1,0]
	v_pk_mul_f32 v[38:39], v[38:39], v[50:51] op_sel_hi:[1,0]
	v_pk_fma_f32 v[2:3], v[76:77], v[42:43], v[26:27]
	v_cvt_pk_bf16_f32 v26, v32, v33
	v_cvt_pk_bf16_f32 v27, v30, v31
	v_pk_fma_f32 v[8:9], v[74:75], v[54:55], v[48:49]
	v_pk_fma_f32 v[6:7], v[72:73], v[52:53], v[46:47]
	v_pk_fma_f32 v[4:5], v[78:79], v[38:39], v[28:29]
	v_cvt_pk_bf16_f32 v28, v36, v37
	v_cvt_pk_bf16_f32 v29, v34, v35
	global_store_dwordx4 v[24:25], v[26:29], off
	s_nop 1
	v_cvt_pk_bf16_f32 v26, v6, v7
	v_cvt_pk_bf16_f32 v27, v8, v9
	v_cvt_pk_bf16_f32 v28, v2, v3
	v_cvt_pk_bf16_f32 v29, v4, v5
	global_store_dwordx4 v[24:25], v[26:29], off offset:1024
	v_mov_b32_e32 v24, v32
	v_mov_b32_e32 v25, v36
	v_mov_b32_e32 v26, v33
	v_mov_b32_e32 v27, v37
	v_pk_mul_f32 v[26:27], v[26:27], v[26:27]
	v_mov_b32_e32 v28, v3
	v_pk_fma_f32 v[24:25], v[24:25], v[24:25], v[26:27]
	v_mov_b32_e32 v26, v30
	v_mov_b32_e32 v27, v34
	v_pk_fma_f32 v[24:25], v[26:27], v[26:27], v[24:25]
	v_mov_b32_e32 v26, v31
	v_mov_b32_e32 v27, v35
	v_mov_b32_e32 v29, v7
	v_pk_fma_f32 v[24:25], v[26:27], v[26:27], v[24:25]
	v_mov_b32_e32 v26, v2
	v_mov_b32_e32 v27, v6
	v_pk_mul_f32 v[28:29], v[28:29], v[28:29]
	v_add_f32_e32 v24, v24, v25
	v_pk_fma_f32 v[26:27], v[26:27], v[26:27], v[28:29]
	v_mov_b32_e32 v28, v4
	v_mov_b32_e32 v29, v8
	v_pk_fma_f32 v[26:27], v[28:29], v[28:29], v[26:27]
	v_mov_b32_e32 v28, v5
	v_mov_b32_e32 v29, v9
	v_pk_fma_f32 v[26:27], v[28:29], v[28:29], v[26:27]
	s_nop 0
	v_add_f32_e32 v24, v27, v24
	v_add_f32_e32 v24, v26, v24
	s_waitcnt lgkmcnt(0)
; #define LAS __attribute__((address_space(3)))
; __device__ __forceinline__ unsigned pk2(float lo, float hi) { unsigned r; asm("v_cvt_pk_bf16_f32 %0, %1, %2" : "=v"(r) : "v"(lo), "v"(hi)); return r; }
; __device__ __forceinline__ float dot2bf(unsigned a, unsigned b, float acc) { return __builtin_amdgcn_fdot2_f32_bf16(__builtin_bit_cast(bf16x2_t, a), __builtin_bit_cast(bf16x2_t, b), acc, false); }
; template <int MODE>
; __device__ __forceinline__ void phase_rowpass1(const Ptrs& P, LAS unsigned char* lds, int layer, int tid_, int vcu, int G) {
;     ...
;         float ss = 0.f;
; #pragma unroll
;         for (int j = 0; j < 4; ++j) ss += v[j][0] * v[j][0] + v[j][1] * v[j][1] + v[j][2] * v[j][2] + v[j][3] * v[j][3];
;         const float rstd = rsqrtf(wave_sum(ss) * (1.f / D) + EPS);
; #pragma unroll
;         for (int j = 0; j < 4; ++j) { const f32x4 g = ((const f32x4*)g1)[F4(j)]; v[j] = v[j] * rstd * g; }
;         if (MODE == 2) {
; #pragma unroll
;             for (int j = 0; j < 4; ++j) ((f32x4*)(P.out + (size_t)row * D))[F4(j)] = v[j];
;         } else {
;             bf16* A = (bf16*)(P.ws + WS_XM) + (size_t)row * D;
;             v4u aw[2];
; #pragma unroll
;             for (int jp = 0; jp < 2; ++jp) { v4u w; w.x = pk2(v[2 * jp][0], v[2 * jp][1]); w.y = pk2(v[2 * jp][2], v[2 * jp][3]); w.z = pk2(v[2 * jp + 1][0], v[2 * jp + 1][1]); w.w = pk2(v[2 * jp + 1][2], v[2 * jp + 1][3]);
;                 ((v4u*)A)[lane + 64 * jp] = w; aw[jp] = w; }
;             float pg[16];
; #pragma unroll
;             for (int g = 0; g < 16; ++g) { float s = 0.f;
; #pragma unroll
;                 for (int jp = 0; jp < 2; ++jp) { const v4u w = *(const LAS v4u*)(gwt + g * 1024 + 8 * lane + 512 * jp); s = dot2bf(aw[jp].x, w.x, s); s = dot2bf(aw[jp].y, w.y, s); s = dot2bf(aw[jp].z, w.z, s); s = dot2bf(aw[jp].w, w.w, s); }
	s_nop 1
	v_add_f32_dpp v24, v24, v24 quad_perm:[1,0,3,2] row_mask:0xf bank_mask:0xf
	s_waitcnt lgkmcnt(0)
	s_nop 1
	v_add_f32_dpp v24, v24, v24 quad_perm:[2,3,0,1] row_mask:0xf bank_mask:0xf
	s_waitcnt lgkmcnt(0)
	s_nop 1
	v_add_f32_dpp v24, v24, v24 row_half_mirror row_mask:0xf bank_mask:0xf
	s_waitcnt lgkmcnt(0)
	s_nop 1
	v_add_f32_dpp v24, v24, v24 row_mirror row_mask:0xf bank_mask:0xf
	v_mov_b32_e32 v25, v24
	s_nop 1
	v_permlane16_swap_b32 v24, v25
	s_waitcnt lgkmcnt(0)
	v_add_f32_e32 v24, v24, v25
	s_nop 0
	s_nop 0
	v_mov_b32_e32 v25, v24
	s_nop 1
	v_permlane32_swap_b32 v24, v25
	s_waitcnt lgkmcnt(0)
	v_add_f32_e32 v24, v24, v25
	v_fmamk_f32 v24, v24, 0x3a800000, v196
	v_cmp_gt_f32_e32 vcc, s73, v24
	v_mul_f32_e32 v25, 0x4b800000, v24
	s_nop 0
	v_cndmask_b32_e32 v24, v24, v25, vcc
	v_rsq_f32_e32 v24, v24
	s_nop 0
	v_mul_f32_e32 v25, 0x45800000, v24
	v_cndmask_b32_e32 v42, v24, v25, vcc
	v_pk_mul_f32 v[28:29], v[32:33], v[42:43] op_sel_hi:[1,0]
	v_pk_mul_f32 v[30:31], v[30:31], v[42:43] op_sel_hi:[1,0]
	v_pk_mul_f32 v[2:3], v[2:3], v[42:43] op_sel_hi:[1,0]
	v_pk_mul_f32 v[4:5], v[4:5], v[42:43] op_sel_hi:[1,0]
	v_add_co_u32_e32 v22, vcc, s25, v22
	v_pk_mul_f32 v[6:7], v[6:7], v[42:43] op_sel_hi:[1,0]
	v_pk_mul_f32 v[8:9], v[8:9], v[42:43] op_sel_hi:[1,0]
	v_addc_co_u32_e32 v23, vcc, 0, v23, vcc
	v_pk_mul_f32 v[32:33], v[82:83], v[30:31]
	v_pk_mul_f32 v[38:39], v[80:81], v[28:29]
	v_pk_mul_f32 v[28:29], v[36:37], v[42:43] op_sel_hi:[1,0]
	v_pk_mul_f32 v[30:31], v[34:35], v[42:43] op_sel_hi:[1,0]
	v_pk_mul_f32 v[36:37], v[84:85], v[28:29]
	v_pk_mul_f32 v[34:35], v[86:87], v[30:31]
	v_mov_b32_e32 v40, v163
	v_mov_b32_e32 v41, v163
	v_pk_mul_f32 v[26:27], v[94:95], v[4:5]
	v_pk_mul_f32 v[4:5], v[92:93], v[2:3]
	v_pk_mul_f32 v[30:31], v[90:91], v[8:9]
	v_cvt_pk_bf16_f32 v4, v4, v5
	v_cvt_pk_bf16_f32 v5, v26, v27
	v_pk_mul_f32 v[28:29], v[88:89], v[6:7]
	v_cvt_pk_bf16_f32 v6, v38, v39
	v_cvt_pk_bf16_f32 v7, v32, v33
	v_cvt_pk_bf16_f32 v8, v36, v37
	v_cvt_pk_bf16_f32 v9, v34, v35
	global_store_dwordx4 v[22:23], v[6:9], off
	v_cvt_pk_bf16_f32 v2, v28, v29
	v_cvt_pk_bf16_f32 v3, v30, v31
	global_store_dwordx4 v[22:23], v[2:5], off offset:1024
	v_mov_b32_e32 v22, v163
	v_dot2c_f32_bf16_e32 v22, v6, v96
	v_dot2c_f32_bf16_e32 v22, v7, v97
	v_dot2c_f32_bf16_e32 v22, v8, v98
	v_dot2c_f32_bf16_e32 v22, v9, v99
	v_mov_b32_e32 v23, v163
	v_mov_b32_e32 v36, v163
	v_mov_b32_e32 v37, v163
	v_mov_b32_e32 v38, v163
	v_dot2c_f32_bf16_e32 v22, v2, v100
	v_dot2c_f32_bf16_e32 v22, v3, v101
	v_dot2c_f32_bf16_e32 v22, v4, v102
	v_dot2c_f32_bf16_e32 v22, v5, v103
	v_mov_b32_e32 v39, v163
	v_dot2c_f32_bf16_e32 v23, v6, v104
	v_dot2c_f32_bf16_e32 v23, v7, v105
	v_dot2c_f32_bf16_e32 v23, v8, v106
	v_dot2c_f32_bf16_e32 v23, v9, v107
	v_dot2c_f32_bf16_e32 v23, v2, v108
	v_dot2c_f32_bf16_e32 v23, v3, v109
	v_dot2c_f32_bf16_e32 v23, v4, v110
	v_dot2c_f32_bf16_e32 v23, v5, v111
	v_mov_b32_e32 v24, v163
	v_mov_b32_e32 v25, v163
	v_dot2c_f32_bf16_e32 v24, v6, v112
	v_dot2c_f32_bf16_e32 v24, v7, v113
	v_dot2c_f32_bf16_e32 v24, v8, v114
	v_dot2c_f32_bf16_e32 v24, v9, v115
	v_dot2c_f32_bf16_e32 v24, v2, v116
	v_dot2c_f32_bf16_e32 v24, v3, v117
	v_dot2c_f32_bf16_e32 v24, v4, v118
	v_dot2c_f32_bf16_e32 v24, v5, v119
	v_dot2c_f32_bf16_e32 v25, v6, v120
	v_dot2c_f32_bf16_e32 v25, v7, v121
	v_dot2c_f32_bf16_e32 v25, v8, v122
	v_dot2c_f32_bf16_e32 v25, v9, v123
	v_dot2c_f32_bf16_e32 v25, v2, v124
	v_dot2c_f32_bf16_e32 v25, v3, v125
	v_dot2c_f32_bf16_e32 v25, v4, v126
	v_dot2c_f32_bf16_e32 v25, v5, v127
	v_mov_b32_e32 v26, v163
	v_mov_b32_e32 v27, v163
	v_dot2c_f32_bf16_e32 v26, v6, v128
	v_dot2c_f32_bf16_e32 v26, v7, v129
	v_dot2c_f32_bf16_e32 v26, v8, v130
	v_dot2c_f32_bf16_e32 v26, v9, v131
	v_dot2c_f32_bf16_e32 v26, v2, v132
	v_dot2c_f32_bf16_e32 v26, v3, v133
	v_dot2c_f32_bf16_e32 v26, v4, v134
	v_dot2c_f32_bf16_e32 v26, v5, v135
	v_dot2c_f32_bf16_e32 v27, v6, v136
	v_dot2c_f32_bf16_e32 v27, v7, v137
	v_dot2c_f32_bf16_e32 v27, v8, v138
	v_dot2c_f32_bf16_e32 v27, v9, v139
	v_dot2c_f32_bf16_e32 v27, v2, v140
	v_dot2c_f32_bf16_e32 v27, v3, v141
	v_dot2c_f32_bf16_e32 v27, v4, v142
	v_dot2c_f32_bf16_e32 v27, v5, v143
	v_mov_b32_e32 v28, v163
	v_mov_b32_e32 v29, v163
	v_dot2c_f32_bf16_e32 v28, v6, v144
	v_dot2c_f32_bf16_e32 v28, v7, v145
	v_dot2c_f32_bf16_e32 v28, v8, v146
	v_dot2c_f32_bf16_e32 v28, v9, v147
	v_dot2c_f32_bf16_e32 v28, v2, v148
	v_dot2c_f32_bf16_e32 v28, v3, v149
	v_dot2c_f32_bf16_e32 v28, v4, v150
	v_dot2c_f32_bf16_e32 v28, v5, v151
	v_dot2c_f32_bf16_e32 v29, v6, v152
	v_dot2c_f32_bf16_e32 v29, v7, v153
	v_dot2c_f32_bf16_e32 v29, v8, v154
	v_dot2c_f32_bf16_e32 v29, v9, v155
	v_dot2c_f32_bf16_e32 v29, v2, v156
	v_dot2c_f32_bf16_e32 v29, v3, v157
	v_dot2c_f32_bf16_e32 v29, v4, v158
	v_dot2c_f32_bf16_e32 v29, v5, v159
	v_mov_b32_e32 v30, v163
	v_mov_b32_e32 v31, v163
	v_dot2c_f32_bf16_e32 v30, v6, v168
	v_dot2c_f32_bf16_e32 v30, v7, v169
	v_dot2c_f32_bf16_e32 v30, v8, v170
	v_dot2c_f32_bf16_e32 v30, v9, v171
	v_dot2c_f32_bf16_e32 v30, v2, v172
	v_dot2c_f32_bf16_e32 v30, v3, v173
	v_dot2c_f32_bf16_e32 v30, v4, v174
	v_dot2c_f32_bf16_e32 v30, v5, v175
	v_dot2c_f32_bf16_e32 v31, v6, v176
	v_dot2c_f32_bf16_e32 v31, v7, v177
	v_dot2c_f32_bf16_e32 v31, v8, v178
	v_dot2c_f32_bf16_e32 v31, v9, v179
	v_dot2c_f32_bf16_e32 v31, v2, v180
	v_dot2c_f32_bf16_e32 v31, v3, v181
	v_dot2c_f32_bf16_e32 v31, v4, v182
	v_dot2c_f32_bf16_e32 v31, v5, v183
	v_dot2c_f32_bf16_e32 v36, v6, v184
	v_dot2c_f32_bf16_e32 v36, v7, v185
	v_dot2c_f32_bf16_e32 v36, v8, v186
	v_dot2c_f32_bf16_e32 v36, v9, v187
	v_dot2c_f32_bf16_e32 v36, v2, v188
	v_dot2c_f32_bf16_e32 v36, v3, v189
	v_dot2c_f32_bf16_e32 v36, v4, v190
	v_dot2c_f32_bf16_e32 v36, v5, v191
	v_dot2c_f32_bf16_e32 v37, v6, v192
	v_dot2c_f32_bf16_e32 v37, v7, v193
	v_dot2c_f32_bf16_e32 v37, v8, v194
	v_dot2c_f32_bf16_e32 v37, v9, v195
	v_dot2c_f32_bf16_e32 v37, v2, v200
	v_dot2c_f32_bf16_e32 v37, v3, v201
	v_dot2c_f32_bf16_e32 v37, v4, v202
	v_dot2c_f32_bf16_e32 v37, v5, v203
	v_dot2c_f32_bf16_e32 v38, v6, v204
	v_dot2c_f32_bf16_e32 v38, v7, v205
	v_dot2c_f32_bf16_e32 v38, v8, v206
	v_dot2c_f32_bf16_e32 v38, v9, v207
	v_dot2c_f32_bf16_e32 v38, v2, v208
	v_dot2c_f32_bf16_e32 v38, v3, v209
	v_dot2c_f32_bf16_e32 v38, v4, v210
	v_dot2c_f32_bf16_e32 v38, v5, v211
	v_dot2c_f32_bf16_e32 v39, v6, v212
	v_dot2c_f32_bf16_e32 v39, v7, v213
	v_dot2c_f32_bf16_e32 v39, v8, v214
	v_dot2c_f32_bf16_e32 v39, v9, v215
	v_dot2c_f32_bf16_e32 v39, v2, v216
	v_dot2c_f32_bf16_e32 v39, v3, v217
	v_dot2c_f32_bf16_e32 v39, v4, v218
	v_dot2c_f32_bf16_e32 v39, v5, v219
	v_dot2c_f32_bf16_e32 v40, v6, v220
	v_dot2c_f32_bf16_e32 v40, v7, v221
	v_dot2c_f32_bf16_e32 v40, v8, v222
	v_dot2c_f32_bf16_e32 v40, v9, v223
	v_dot2c_f32_bf16_e32 v40, v2, v224
	v_dot2c_f32_bf16_e32 v40, v3, v225
	v_dot2c_f32_bf16_e32 v40, v4, v226
	v_dot2c_f32_bf16_e32 v40, v5, v227
	v_dot2c_f32_bf16_e32 v41, v6, v228
	v_dot2c_f32_bf16_e32 v41, v7, v229
	v_dot2c_f32_bf16_e32 v41, v8, v230
	v_dot2c_f32_bf16_e32 v41, v9, v231
	ds_read_b128 v[6:9], v11 offset:31744
	s_waitcnt lgkmcnt(0)
; #define LAS __attribute__((address_space(3)))
; __device__ __forceinline__ float logsigf_(float x) { return fminf(x, 0.f) - __logf(1.f + __expf(-fabsf(x))); }
; #define SHX(v, m) (((m) < 32) ? __int_as_float(__builtin_amdgcn_ds_swizzle(__float_as_int(v), ((((m) & 31) << 10) | 0x1f))) : shx32(v))
; __device__ __forceinline__ float dot2bf(unsigned a, unsigned b, float acc) { return __builtin_amdgcn_fdot2_f32_bf16(__builtin_bit_cast(bf16x2_t, a), __builtin_bit_cast(bf16x2_t, b), acc, false); }
; template <int MODE>
; __device__ __forceinline__ void phase_rowpass1(const Ptrs& P, LAS unsigned char* lds, int layer, int tid_, int vcu, int G) {
;     ...
;                 for (int jp = 0; jp < 2; ++jp) { const v4u w = *(const LAS v4u*)(gwt + g * 1024 + 8 * lane + 512 * jp); s = dot2bf(aw[jp].x, w.x, s); s = dot2bf(aw[jp].y, w.y, s); s = dot2bf(aw[jp].z, w.z, s); s = dot2bf(aw[jp].w, w.w, s); }
;                 pg[g] = s; }
;             float p8[8], p4[4], p2[2], p1;
;             { const bool hi = (lane & 32) != 0;
; #pragma unroll
;               for (int i = 0; i < 8; ++i) { const float send = hi ? pg[i] : pg[8 + i], keep = hi ? pg[8 + i] : pg[i]; p8[i] = keep + SHX(send, 32); } }
;             { const bool hi = (lane & 16) != 0;
; #pragma unroll
;               for (int i = 0; i < 4; ++i) { const float send = hi ? p8[i] : p8[4 + i], keep = hi ? p8[4 + i] : p8[i]; p4[i] = keep + SHX(send, 16); } }
;             { const bool hi = (lane & 8) != 0;
; #pragma unroll
;               for (int i = 0; i < 2; ++i) { const float send = hi ? p4[i] : p4[2 + i], keep = hi ? p4[2 + i] : p4[i]; p2[i] = keep + SHX(send, 8); } }
;             { const bool hi = (lane & 4) != 0; const float send = hi ? p2[0] : p2[1], keep = hi ? p2[1] : p2[0]; p1 = keep + SHX(send, 4); }
;             p1 += SHX(p1, 2); p1 += SHX(p1, 1);
;             const int src = (((lane >> 3) & 1) << 5) | (((lane >> 2) & 1) << 4) | (((lane >> 1) & 1) << 3) | ((lane & 1) << 2);
;             const float mine = __int_as_float(__builtin_amdgcn_ds_bpermute(src << 2, __float_as_int(p1)));
;             if (lane < 16) { float gv = mine + P.gate_b[layer * 16 + lane]; if ((lane >> 2) & 1) gv = logsigf_(gv); ((float*)(P.ws + WS_GATES))[(size_t)row * 16 + lane] = gv; }
	v_dot2c_f32_bf16_e32 v41, v2, v6
	v_dot2c_f32_bf16_e32 v41, v3, v7
	v_dot2c_f32_bf16_e32 v41, v4, v8
	v_mbcnt_lo_u32_b32 v4, -1, 0
	v_cndmask_b32_e64 v2, v22, v30, s[38:39]
	v_mbcnt_hi_u32_b32 v4, -1, v4
	v_dot2c_f32_bf16_e32 v41, v5, v9
	v_lshlrev_b32_e32 v4, 2, v4
	v_xor_b32_e32 v4, 0x80, v4
	ds_bpermute_b32 v2, v4, v2
	v_mbcnt_lo_u32_b32 v5, -1, 0
	v_cndmask_b32_e64 v3, v30, v22, s[38:39]
	v_mbcnt_hi_u32_b32 v5, -1, v5
	v_mbcnt_lo_u32_b32 v6, -1, 0
	s_waitcnt lgkmcnt(0)
	v_add_f32_e32 v2, v3, v2
	v_lshlrev_b32_e32 v5, 2, v5
	v_cndmask_b32_e64 v3, v23, v31, s[38:39]
	v_xor_b32_e32 v5, 0x80, v5
	ds_bpermute_b32 v3, v5, v3
	v_mbcnt_hi_u32_b32 v6, -1, v6
	v_cndmask_b32_e64 v4, v31, v23, s[38:39]
	v_lshlrev_b32_e32 v6, 2, v6
	v_xor_b32_e32 v6, 0x80, v6
	s_waitcnt lgkmcnt(0)
	v_add_f32_e32 v3, v4, v3
	v_cndmask_b32_e64 v4, v24, v36, s[38:39]
	ds_bpermute_b32 v4, v6, v4
	v_mbcnt_lo_u32_b32 v7, -1, 0
	v_cndmask_b32_e64 v5, v36, v24, s[38:39]
	v_mbcnt_hi_u32_b32 v7, -1, v7
	v_mbcnt_lo_u32_b32 v8, -1, 0
	s_waitcnt lgkmcnt(0)
	v_add_f32_e32 v4, v5, v4
	v_lshlrev_b32_e32 v7, 2, v7
	v_cndmask_b32_e64 v5, v25, v37, s[38:39]
	v_xor_b32_e32 v7, 0x80, v7
	ds_bpermute_b32 v5, v7, v5
	v_mbcnt_hi_u32_b32 v8, -1, v8
	v_cndmask_b32_e64 v6, v37, v25, s[38:39]
	v_lshlrev_b32_e32 v8, 2, v8
	v_xor_b32_e32 v8, 0x80, v8
	s_waitcnt lgkmcnt(0)
	v_add_f32_e32 v5, v6, v5
	v_cndmask_b32_e64 v6, v26, v38, s[38:39]
	ds_bpermute_b32 v6, v8, v6
	v_mbcnt_lo_u32_b32 v9, -1, 0
	v_cndmask_b32_e64 v7, v38, v26, s[38:39]
	v_mbcnt_hi_u32_b32 v9, -1, v9
	v_mbcnt_lo_u32_b32 v22, -1, 0
	s_waitcnt lgkmcnt(0)
	v_add_f32_e32 v6, v7, v6
	v_lshlrev_b32_e32 v9, 2, v9
	v_cndmask_b32_e64 v7, v27, v39, s[38:39]
	v_xor_b32_e32 v9, 0x80, v9
	ds_bpermute_b32 v7, v9, v7
	v_mbcnt_hi_u32_b32 v22, -1, v22
	v_cndmask_b32_e64 v8, v39, v27, s[38:39]
	v_lshlrev_b32_e32 v22, 2, v22
	v_xor_b32_e32 v22, 0x80, v22
	s_waitcnt lgkmcnt(0)
	v_add_f32_e32 v7, v8, v7
	v_cndmask_b32_e64 v8, v28, v40, s[38:39]
	ds_bpermute_b32 v8, v22, v8
	v_mbcnt_lo_u32_b32 v23, -1, 0
	v_cndmask_b32_e64 v9, v40, v28, s[38:39]
	v_mbcnt_hi_u32_b32 v23, -1, v23
	v_cndmask_b32_e64 v22, v41, v29, s[38:39]
	v_lshlrev_b32_e32 v23, 2, v23
	s_waitcnt lgkmcnt(0)
	v_add_f32_e32 v8, v9, v8
	v_cndmask_b32_e64 v9, v29, v41, s[38:39]
	v_xor_b32_e32 v23, 0x80, v23
	ds_bpermute_b32 v9, v23, v9
	s_waitcnt lgkmcnt(0)
	v_add_f32_e32 v9, v22, v9
	v_cndmask_b32_e64 v22, v2, v6, s[40:41]
	v_cndmask_b32_e64 v2, v6, v2, s[40:41]
	ds_swizzle_b32 v6, v22 offset:swizzle(SWAP,16)
	s_waitcnt lgkmcnt(0)
	v_add_f32_e32 v2, v2, v6
	v_cndmask_b32_e64 v6, v3, v7, s[40:41]
	ds_swizzle_b32 v6, v6 offset:swizzle(SWAP,16)
	v_cndmask_b32_e64 v3, v7, v3, s[40:41]
	s_waitcnt lgkmcnt(0)
	v_add_f32_e32 v3, v3, v6
	v_cndmask_b32_e64 v6, v4, v8, s[40:41]
	ds_swizzle_b32 v6, v6 offset:swizzle(SWAP,16)
	v_cndmask_b32_e64 v4, v8, v4, s[40:41]
	s_waitcnt lgkmcnt(0)
	v_add_f32_e32 v4, v4, v6
	v_cndmask_b32_e64 v6, v5, v9, s[40:41]
	ds_swizzle_b32 v6, v6 offset:swizzle(SWAP,16)
	v_cndmask_b32_e64 v5, v9, v5, s[40:41]
	s_waitcnt lgkmcnt(0)
	v_add_f32_e32 v5, v5, v6
	v_cndmask_b32_e64 v6, v2, v4, s[42:43]
	v_cndmask_b32_e64 v2, v4, v2, s[42:43]
	ds_swizzle_b32 v4, v6 offset:swizzle(SWAP,8)
	s_waitcnt lgkmcnt(0)
	v_add_f32_e32 v2, v2, v4
	v_cndmask_b32_e64 v4, v3, v5, s[42:43]
	ds_swizzle_b32 v4, v4 offset:swizzle(SWAP,8)
	v_cndmask_b32_e64 v3, v5, v3, s[42:43]
	s_waitcnt lgkmcnt(0)
	v_add_f32_e32 v3, v3, v4
	v_cndmask_b32_e64 v4, v2, v3, s[44:45]
	v_cndmask_b32_e64 v2, v3, v2, s[44:45]
	ds_swizzle_b32 v3, v4 offset:swizzle(SWAP,4)
	s_waitcnt lgkmcnt(0)
	v_add_f32_e32 v2, v2, v3
	ds_swizzle_b32 v3, v2 offset:swizzle(SWAP,2)
	s_waitcnt lgkmcnt(0)
	v_add_f32_e32 v2, v2, v3
	s_waitcnt lgkmcnt(0)
	s_nop 1
	v_add_f32_dpp v2, v2, v2 quad_perm:[1,0,3,2] row_mask:0xf bank_mask:0xf
	ds_bpermute_b32 v2, v1, v2
	s_and_saveexec_b64 s[8:9], s[46:47]
	s_cbranch_execz .LBB0_265
	s_waitcnt lgkmcnt(0)
	v_add_f32_e32 v2, v246, v2
	s_and_saveexec_b64 s[18:19], s[48:49]
	s_cbranch_execz .LBB0_264
	s_mov_b32 s4, 0xbfb8aa3b
	v_mul_f32_e64 v3, |v2|, s4
	v_exp_f32_e32 v3, v3
	s_mov_b32 s4, 0x3f317217
	v_max_f32_e32 v2, v2, v2
	v_min_f32_e32 v2, 0, v2
	v_add_f32_e32 v3, 1.0, v3
	v_cmp_gt_f32_e32 vcc, s73, v3
	s_nop 1
	v_cndmask_b32_e64 v4, 0, 32, vcc
	v_ldexp_f32 v3, v3, v4
	v_log_f32_e32 v3, v3
	s_nop 0
	v_mul_f32_e32 v4, 0x3f317217, v3
	v_fma_f32 v4, v3, s4, -v4
	v_fmac_f32_e32 v4, 0x3377d1cf, v3
	s_mov_b32 s4, 0x7f800000
	v_fmac_f32_e32 v4, 0x3f317217, v3
	v_cmp_lt_f32_e64 s[50:51], |v3|, s4
	s_nop 1
	v_cndmask_b32_e64 v3, v3, v4, s[50:51]
	v_cndmask_b32_e32 v4, 0, v247, vcc
	v_sub_f32_e32 v3, v3, v4
	v_sub_f32_e32 v2, v2, v3
	s_branch .LBB0_264

; __device__ __forceinline__ unsigned pk2(float lo, float hi) { unsigned r; asm("v_cvt_pk_bf16_f32 %0, %1, %2" : "=v"(r) : "v"(lo), "v"(hi)); return r; }
; __device__ __forceinline__ float bflo(unsigned w) { return __uint_as_float(w << 16); }
; __device__ __forceinline__ float bfhi(unsigned w) { return __uint_as_float(w & 0xffff0000u); }
; template <int MODE>
; __device__ __forceinline__ void phase_rowpass1(const Ptrs& P, LAS unsigned char* lds, int layer, int tid_, int vcu, int G) {
;     ...
;     for (int row = gw; row < T; row += NGW) {
;         f32x4 v[4];
;         if (MODE == 0) {
; #pragma unroll
;             for (int j = 0; j < 4; ++j) v[j] = ((const f32x4*)(P.x + (size_t)row * D))[F4(j)];
;         } else {
;             f32x4 e[4]; float ss = 0.f;
; #pragma unroll
;             for (int jp = 0; jp < 2; ++jp) { const v4u hw = ((const v4u*)(H + (size_t)row * D))[lane + 64 * jp]; const v4u w = __builtin_nontemporal_load((const v4u*)(GE + (size_t)row * D) + lane + 64 * jp);
;                 v[2 * jp] = (f32x4){bflo(hw.x), bfhi(hw.x), bflo(hw.y), bfhi(hw.y)}; v[2 * jp + 1] = (f32x4){bflo(hw.z), bfhi(hw.z), bflo(hw.w), bfhi(hw.w)};
;                 e[2 * jp] = (f32x4){bflo(w.x), bfhi(w.x), bflo(w.y), bfhi(w.y)}; e[2 * jp + 1] = (f32x4){bflo(w.z), bfhi(w.z), bflo(w.w), bfhi(w.w)}; }
; #pragma unroll
;             for (int j = 0; j < 4; ++j) ss += e[j][0] * e[j][0] + e[j][1] * e[j][1] + e[j][2] * e[j][2] + e[j][3] * e[j][3];
;             const float r = rsqrtf(wave_sum(ss) * (1.f / D) + EPS);
; #pragma unroll
;             for (int j = 0; j < 4; ++j) { const f32x4 g = ((const f32x4*)pg)[F4(j)]; v[j] = v[j] + e[j] * r * g; }
;         }
;         if (MODE != 2) {
; #pragma unroll
;             for (int jp = 0; jp < 2; ++jp) { v4u hw; hw.x = pk2(v[2 * jp][0], v[2 * jp][1]); hw.y = pk2(v[2 * jp][2], v[2 * jp][3]); hw.z = pk2(v[2 * jp + 1][0], v[2 * jp + 1][1]); hw.w = pk2(v[2 * jp + 1][2], v[2 * jp + 1][3]);
;                 ((v4u*)(H + (size_t)row * D))[lane + 64 * jp] = hw; }
;         }
;         float ss = 0.f;
; #pragma unroll
;         for (int j = 0; j < 4; ++j) ss += v[j][0] * v[j][0] + v[j][1] * v[j][1] + v[j][2] * v[j][2] + v[j][3] * v[j][3];
;         const float rstd = rsqrtf(wave_sum(ss) * (1.f / D) + EPS);
; #pragma unroll
;         for (int j = 0; j < 4; ++j) { const f32x4 g = ((const f32x4*)g1)[F4(j)]; v[j] = v[j] * rstd * g; }
.LBB0_279:
	global_load_dwordx4 v[10:13], v[28:29], off offset:-2048
	global_load_dwordx4 v[14:17], v[28:29], off offset:-2064
	s_waitcnt lgkmcnt(0)
	global_load_dwordx4 v[2:5], v[28:29], off
	global_load_dwordx4 v[6:9], v[28:29], off offset:-16
	v_lshl_add_u64 v[30:31], s[0:1], 0, v[26:27]
	s_mov_b32 s4, 0x34600000
	v_add_co_u32_e64 v38, s[48:49], s4, v30
	s_waitcnt vmcnt(3)
	v_cvt_pk_bf16_f32 v36, v10, v11
	v_cvt_pk_bf16_f32 v37, v12, v13
	s_nop 0
	v_addc_co_u32_e64 v39, s[48:49], 0, v31, s[48:49]
	s_waitcnt vmcnt(2)
	v_cvt_pk_bf16_f32 v34, v14, v15
	v_cvt_pk_bf16_f32 v35, v16, v17
	global_store_dwordx4 v[38:39], v[34:37], off
	s_waitcnt vmcnt(2)
	s_nop 0
	v_cvt_pk_bf16_f32 v36, v2, v3
	v_cvt_pk_bf16_f32 v37, v4, v5
	s_waitcnt vmcnt(1)
	v_cvt_pk_bf16_f32 v34, v6, v7
	v_cvt_pk_bf16_f32 v35, v8, v9
	global_store_dwordx4 v[38:39], v[34:37], off offset:1024
	v_mov_b32_e32 v38, v7
	v_mov_b32_e32 v39, v3
	v_mov_b32_e32 v36, v15
	v_mov_b32_e32 v37, v11
	v_mov_b32_e32 v34, v14
	v_mov_b32_e32 v35, v10
	v_pk_mul_f32 v[36:37], v[36:37], v[36:37]
	v_pk_mul_f32 v[38:39], v[38:39], v[38:39]
	v_pk_fma_f32 v[34:35], v[34:35], v[34:35], v[36:37]
	v_mov_b32_e32 v36, v16
	v_mov_b32_e32 v37, v12
	v_pk_fma_f32 v[34:35], v[36:37], v[36:37], v[34:35]
	v_mov_b32_e32 v36, v17
	v_mov_b32_e32 v37, v13
	v_pk_fma_f32 v[34:35], v[36:37], v[36:37], v[34:35]
	v_mov_b32_e32 v36, v6
	v_mov_b32_e32 v37, v2
	v_pk_fma_f32 v[36:37], v[36:37], v[36:37], v[38:39]
	v_mov_b32_e32 v38, v8
	v_mov_b32_e32 v39, v4
	v_pk_fma_f32 v[36:37], v[38:39], v[38:39], v[36:37]
	v_mov_b32_e32 v38, v9
	v_mov_b32_e32 v39, v5
	v_pk_fma_f32 v[36:37], v[38:39], v[38:39], v[36:37]
	v_add_f32_e32 v19, v34, v35
	v_add_f32_e32 v19, v19, v36
	v_add_f32_e32 v19, v19, v37
	s_waitcnt lgkmcnt(0)
	s_nop 1
	v_add_f32_dpp v19, v19, v19 quad_perm:[1,0,3,2] row_mask:0xf bank_mask:0xf
	s_waitcnt lgkmcnt(0)
	s_nop 1
	v_add_f32_dpp v19, v19, v19 quad_perm:[2,3,0,1] row_mask:0xf bank_mask:0xf
	s_waitcnt lgkmcnt(0)
	s_nop 1
	v_add_f32_dpp v19, v19, v19 row_half_mirror row_mask:0xf bank_mask:0xf
	s_waitcnt lgkmcnt(0)
	s_nop 1
	v_add_f32_dpp v19, v19, v19 row_mirror row_mask:0xf bank_mask:0xf
	v_mov_b32_e32 v33, v19
	s_nop 1
	v_permlane16_swap_b32 v19, v33
	s_waitcnt lgkmcnt(0)
	v_add_f32_e32 v19, v19, v33
	v_mbcnt_lo_u32_b32 v33, -1, 0
	s_nop 0
	v_mbcnt_hi_u32_b32 v33, -1, v33
	global_load_dwordx4 v[34:37], v[20:21], off offset:16
	global_load_dwordx4 v[38:41], v[20:21], off
	v_lshlrev_b32_e32 v33, 2, v33
	v_xor_b32_e32 v33, 0x80, v33
	ds_bpermute_b32 v33, v33, v19
	s_waitcnt lgkmcnt(0)
	v_add_f32_e32 v19, v19, v33
	v_fmamk_f32 v19, v19, 0x3a800000, v196
	v_cmp_gt_f32_e64 s[48:49], s73, v19
	v_mul_f32_e32 v33, 0x4b800000, v19
	s_nop 0
	v_cndmask_b32_e64 v19, v19, v33, s[48:49]
	v_rsq_f32_e32 v19, v19
	s_nop 0
	v_mul_f32_e32 v33, 0x45800000, v19
	v_cndmask_b32_e64 v42, v19, v33, s[48:49]
	v_pk_mul_f32 v[14:15], v[14:15], v[42:43] op_sel_hi:[1,0]
	v_pk_mul_f32 v[16:17], v[16:17], v[42:43] op_sel_hi:[1,0]
	v_pk_mul_f32 v[10:11], v[10:11], v[42:43] op_sel_hi:[1,0]
	v_pk_mul_f32 v[12:13], v[12:13], v[42:43] op_sel_hi:[1,0]
	v_pk_mul_f32 v[2:3], v[2:3], v[42:43] op_sel_hi:[1,0]
	v_pk_mul_f32 v[4:5], v[4:5], v[42:43] op_sel_hi:[1,0]
	v_pk_mul_f32 v[6:7], v[6:7], v[42:43] op_sel_hi:[1,0]
	v_pk_mul_f32 v[8:9], v[8:9], v[42:43] op_sel_hi:[1,0]
	v_mov_b32_e32 v19, v163
	v_mov_b32_e32 v33, v163
	v_mov_b32_e32 v42, v163
	s_waitcnt vmcnt(1)
	v_pk_mul_f32 v[36:37], v[36:37], v[12:13]
	s_waitcnt vmcnt(0)
	v_pk_mul_f32 v[40:41], v[40:41], v[16:17]
	v_pk_mul_f32 v[38:39], v[38:39], v[14:15]
	v_pk_mul_f32 v[34:35], v[34:35], v[10:11]
	global_load_dwordx4 v[10:13], v[20:21], off offset:2064
	global_load_dwordx4 v[14:17], v[20:21], off offset:2048
	s_waitcnt vmcnt(1)
	v_pk_mul_f32 v[12:13], v[12:13], v[4:5]
	v_pk_mul_f32 v[4:5], v[10:11], v[2:3]
	v_add_co_u32_e64 v10, s[48:49], s25, v30
	s_waitcnt vmcnt(0)
	v_pk_mul_f32 v[16:17], v[16:17], v[8:9]
	v_addc_co_u32_e64 v11, s[48:49], 0, v31, s[48:49]
	v_pk_mul_f32 v[14:15], v[14:15], v[6:7]
	v_cvt_pk_bf16_f32 v6, v38, v39
	v_cvt_pk_bf16_f32 v7, v40, v41
	v_cvt_pk_bf16_f32 v8, v34, v35
	v_cvt_pk_bf16_f32 v9, v36, v37
	global_store_dwordx4 v[10:11], v[6:9], off
	v_cvt_pk_bf16_f32 v2, v14, v15
	v_cvt_pk_bf16_f32 v3, v16, v17
	v_cvt_pk_bf16_f32 v4, v4, v5
	v_cvt_pk_bf16_f32 v5, v12, v13
	global_store_dwordx4 v[10:11], v[2:5], off offset:1024
	v_add_u32_e32 v11, 0, v1
	ds_read_b128 v[12:15], v11
	ds_read_b128 v[34:37], v11 offset:6144
	v_mov_b32_e32 v10, v163
	v_mov_b32_e32 v30, v163
	v_mov_b32_e32 v31, v163
	s_waitcnt lgkmcnt(1)
	v_dot2c_f32_bf16_e32 v10, v6, v12
	v_dot2c_f32_bf16_e32 v10, v7, v13
	v_dot2c_f32_bf16_e32 v10, v8, v14
	v_dot2c_f32_bf16_e32 v10, v9, v15
	ds_read_b128 v[12:15], v11 offset:1024
	v_mov_b32_e32 v38, v163
	v_mov_b32_e32 v39, v163
	v_mov_b32_e32 v40, v163
	v_mov_b32_e32 v41, v163
	s_waitcnt lgkmcnt(0)
	v_dot2c_f32_bf16_e32 v10, v2, v12
	v_dot2c_f32_bf16_e32 v10, v3, v13
	v_dot2c_f32_bf16_e32 v10, v4, v14
	v_dot2c_f32_bf16_e32 v10, v5, v15
	ds_read_b128 v[14:17], v11 offset:2048
	v_mov_b32_e32 v12, v163
	v_mov_b32_e32 v13, v163
	s_waitcnt lgkmcnt(0)
	v_dot2c_f32_bf16_e32 v12, v6, v14
	v_dot2c_f32_bf16_e32 v12, v7, v15
	v_dot2c_f32_bf16_e32 v12, v8, v16
	v_dot2c_f32_bf16_e32 v12, v9, v17
	ds_read_b128 v[14:17], v11 offset:3072
	s_waitcnt lgkmcnt(0)
	v_dot2c_f32_bf16_e32 v12, v2, v14
	v_dot2c_f32_bf16_e32 v12, v3, v15
	v_dot2c_f32_bf16_e32 v12, v4, v16
	v_dot2c_f32_bf16_e32 v12, v5, v17
	ds_read_b128 v[14:17], v11 offset:4096
	s_waitcnt lgkmcnt(0)
	v_dot2c_f32_bf16_e32 v13, v6, v14
	v_dot2c_f32_bf16_e32 v13, v7, v15
	v_dot2c_f32_bf16_e32 v13, v8, v16
	v_dot2c_f32_bf16_e32 v13, v9, v17
	ds_read_b128 v[14:17], v11 offset:5120
	s_waitcnt lgkmcnt(0)
; #define LAS __attribute__((address_space(3)))
; __device__ __forceinline__ float dot2bf(unsigned a, unsigned b, float acc) { return __builtin_amdgcn_fdot2_f32_bf16(__builtin_bit_cast(bf16x2_t, a), __builtin_bit_cast(bf16x2_t, b), acc, false); }
; template <int MODE>
; __device__ __forceinline__ void phase_rowpass1(const Ptrs& P, LAS unsigned char* lds, int layer, int tid_, int vcu, int G) {
;     ...
;             for (int g = 0; g < 16; ++g) { float s = 0.f;
; #pragma unroll
;                 for (int jp = 0; jp < 2; ++jp) { const v4u w = *(const LAS v4u*)(gwt + g * 1024 + 8 * lane + 512 * jp); s = dot2bf(aw[jp].x, w.x, s); s = dot2bf(aw[jp].y, w.y, s); s = dot2bf(aw[jp].z, w.z, s); s = dot2bf(aw[jp].w, w.w, s); }
;                 pg[g] = s; }
	v_dot2c_f32_bf16_e32 v13, v2, v14
	v_mov_b32_e32 v14, v163
	v_dot2c_f32_bf16_e32 v14, v6, v34
	v_dot2c_f32_bf16_e32 v14, v7, v35
	v_dot2c_f32_bf16_e32 v14, v8, v36
	v_dot2c_f32_bf16_e32 v14, v9, v37
	ds_read_b128 v[34:37], v11 offset:7168
	v_dot2c_f32_bf16_e32 v13, v3, v15
	v_mov_b32_e32 v15, v163
	v_dot2c_f32_bf16_e32 v13, v4, v16
	v_mov_b32_e32 v16, v163
	s_waitcnt lgkmcnt(0)
	v_dot2c_f32_bf16_e32 v14, v2, v34
	v_dot2c_f32_bf16_e32 v14, v3, v35
	v_dot2c_f32_bf16_e32 v14, v4, v36
	v_dot2c_f32_bf16_e32 v14, v5, v37
	ds_read_b128 v[34:37], v11 offset:8192
	v_dot2c_f32_bf16_e32 v13, v5, v17
	v_mov_b32_e32 v17, v163
	s_waitcnt lgkmcnt(0)
	v_dot2c_f32_bf16_e32 v15, v6, v34
	v_dot2c_f32_bf16_e32 v15, v7, v35
	v_dot2c_f32_bf16_e32 v15, v8, v36
	v_dot2c_f32_bf16_e32 v15, v9, v37
	ds_read_b128 v[34:37], v11 offset:9216
	s_waitcnt lgkmcnt(0)
	v_dot2c_f32_bf16_e32 v15, v2, v34
	v_dot2c_f32_bf16_e32 v15, v3, v35
	v_dot2c_f32_bf16_e32 v15, v4, v36
	v_dot2c_f32_bf16_e32 v15, v5, v37
	ds_read_b128 v[34:37], v11 offset:10240
	s_waitcnt lgkmcnt(0)
	v_dot2c_f32_bf16_e32 v16, v6, v34
	v_dot2c_f32_bf16_e32 v16, v7, v35
	v_dot2c_f32_bf16_e32 v16, v8, v36
	v_dot2c_f32_bf16_e32 v16, v9, v37
	ds_read_b128 v[34:37], v11 offset:11264
	s_waitcnt lgkmcnt(0)
	v_dot2c_f32_bf16_e32 v16, v2, v34
	v_dot2c_f32_bf16_e32 v16, v3, v35
	v_dot2c_f32_bf16_e32 v16, v4, v36
	v_dot2c_f32_bf16_e32 v16, v5, v37
	ds_read_b128 v[34:37], v11 offset:12288
	s_waitcnt lgkmcnt(0)
	v_dot2c_f32_bf16_e32 v17, v6, v34
	v_dot2c_f32_bf16_e32 v17, v7, v35
	v_dot2c_f32_bf16_e32 v17, v8, v36
	v_dot2c_f32_bf16_e32 v17, v9, v37
	ds_read_b128 v[34:37], v11 offset:13312
	s_waitcnt lgkmcnt(0)
	v_dot2c_f32_bf16_e32 v17, v2, v34
	v_dot2c_f32_bf16_e32 v17, v3, v35
	v_dot2c_f32_bf16_e32 v17, v4, v36
	v_dot2c_f32_bf16_e32 v17, v5, v37
	ds_read_b128 v[34:37], v11 offset:14336
	s_waitcnt lgkmcnt(0)
	v_dot2c_f32_bf16_e32 v19, v6, v34
	v_dot2c_f32_bf16_e32 v19, v7, v35
	v_dot2c_f32_bf16_e32 v19, v8, v36
	v_dot2c_f32_bf16_e32 v19, v9, v37
	ds_read_b128 v[34:37], v11 offset:15360
	s_waitcnt lgkmcnt(0)
	v_dot2c_f32_bf16_e32 v19, v2, v34
	v_dot2c_f32_bf16_e32 v19, v3, v35
	v_dot2c_f32_bf16_e32 v19, v4, v36
	v_dot2c_f32_bf16_e32 v19, v5, v37
	ds_read_b128 v[34:37], v11 offset:16384
	s_waitcnt lgkmcnt(0)
	v_dot2c_f32_bf16_e32 v30, v6, v34
	v_dot2c_f32_bf16_e32 v30, v7, v35
	v_dot2c_f32_bf16_e32 v30, v8, v36
	v_dot2c_f32_bf16_e32 v30, v9, v37
	ds_read_b128 v[34:37], v11 offset:17408
	s_waitcnt lgkmcnt(0)
	v_dot2c_f32_bf16_e32 v30, v2, v34
	v_dot2c_f32_bf16_e32 v30, v3, v35
	v_dot2c_f32_bf16_e32 v30, v4, v36
	v_dot2c_f32_bf16_e32 v30, v5, v37
	ds_read_b128 v[34:37], v11 offset:18432
	s_waitcnt lgkmcnt(0)
	v_dot2c_f32_bf16_e32 v31, v6, v34
	v_dot2c_f32_bf16_e32 v31, v7, v35
	v_dot2c_f32_bf16_e32 v31, v8, v36
	v_dot2c_f32_bf16_e32 v31, v9, v37
	ds_read_b128 v[34:37], v11 offset:19456
	s_waitcnt lgkmcnt(0)
	v_dot2c_f32_bf16_e32 v31, v2, v34
	v_dot2c_f32_bf16_e32 v31, v3, v35
	v_dot2c_f32_bf16_e32 v31, v4, v36
	v_dot2c_f32_bf16_e32 v31, v5, v37
	ds_read_b128 v[34:37], v11 offset:20480
	s_waitcnt lgkmcnt(0)
	v_dot2c_f32_bf16_e32 v33, v6, v34
	v_dot2c_f32_bf16_e32 v33, v7, v35
	v_dot2c_f32_bf16_e32 v33, v8, v36
	v_dot2c_f32_bf16_e32 v33, v9, v37
	ds_read_b128 v[34:37], v11 offset:21504
	s_waitcnt lgkmcnt(0)
	v_dot2c_f32_bf16_e32 v33, v2, v34
	v_dot2c_f32_bf16_e32 v33, v3, v35
	v_dot2c_f32_bf16_e32 v33, v4, v36
	v_dot2c_f32_bf16_e32 v33, v5, v37
	ds_read_b128 v[34:37], v11 offset:22528
	s_waitcnt lgkmcnt(0)
	v_dot2c_f32_bf16_e32 v38, v6, v34
	v_dot2c_f32_bf16_e32 v38, v7, v35
	v_dot2c_f32_bf16_e32 v38, v8, v36
	v_dot2c_f32_bf16_e32 v38, v9, v37
	ds_read_b128 v[34:37], v11 offset:23552
	s_waitcnt lgkmcnt(0)
	v_dot2c_f32_bf16_e32 v38, v2, v34
	v_dot2c_f32_bf16_e32 v38, v3, v35
	v_dot2c_f32_bf16_e32 v38, v4, v36
	v_dot2c_f32_bf16_e32 v38, v5, v37
	ds_read_b128 v[34:37], v11 offset:24576
	s_waitcnt lgkmcnt(0)
	v_dot2c_f32_bf16_e32 v39, v6, v34
	v_dot2c_f32_bf16_e32 v39, v7, v35
	v_dot2c_f32_bf16_e32 v39, v8, v36
	v_dot2c_f32_bf16_e32 v39, v9, v37
	ds_read_b128 v[34:37], v11 offset:25600
	s_waitcnt lgkmcnt(0)
	v_dot2c_f32_bf16_e32 v39, v2, v34
	v_dot2c_f32_bf16_e32 v39, v3, v35
	v_dot2c_f32_bf16_e32 v39, v4, v36
	v_dot2c_f32_bf16_e32 v39, v5, v37
	ds_read_b128 v[34:37], v11 offset:26624
	s_waitcnt lgkmcnt(0)
	v_dot2c_f32_bf16_e32 v40, v6, v34
	v_dot2c_f32_bf16_e32 v40, v7, v35
	v_dot2c_f32_bf16_e32 v40, v8, v36
	v_dot2c_f32_bf16_e32 v40, v9, v37
	ds_read_b128 v[34:37], v11 offset:27648
	s_waitcnt lgkmcnt(0)
	v_dot2c_f32_bf16_e32 v40, v2, v34
	v_dot2c_f32_bf16_e32 v40, v3, v35
	v_dot2c_f32_bf16_e32 v40, v4, v36
	v_dot2c_f32_bf16_e32 v40, v5, v37
	ds_read_b128 v[34:37], v11 offset:28672
	s_waitcnt lgkmcnt(0)
	v_dot2c_f32_bf16_e32 v41, v6, v34
	v_dot2c_f32_bf16_e32 v41, v7, v35
	v_dot2c_f32_bf16_e32 v41, v8, v36
	v_dot2c_f32_bf16_e32 v41, v9, v37
	ds_read_b128 v[34:37], v11 offset:29696
	s_waitcnt lgkmcnt(0)
; #define LAS __attribute__((address_space(3)))
; __device__ __forceinline__ float logsigf_(float x) { return fminf(x, 0.f) - __logf(1.f + __expf(-fabsf(x))); }
; #define SHX(v, m) (((m) < 32) ? __int_as_float(__builtin_amdgcn_ds_swizzle(__float_as_int(v), ((((m) & 31) << 10) | 0x1f))) : shx32(v))
; __device__ __forceinline__ float dot2bf(unsigned a, unsigned b, float acc) { return __builtin_amdgcn_fdot2_f32_bf16(__builtin_bit_cast(bf16x2_t, a), __builtin_bit_cast(bf16x2_t, b), acc, false); }
; template <int MODE>
; __device__ __forceinline__ void phase_rowpass1(const Ptrs& P, LAS unsigned char* lds, int layer, int tid_, int vcu, int G) {
;     ...
;             for (int g = 0; g < 16; ++g) { float s = 0.f;
; #pragma unroll
;                 for (int jp = 0; jp < 2; ++jp) { const v4u w = *(const LAS v4u*)(gwt + g * 1024 + 8 * lane + 512 * jp); s = dot2bf(aw[jp].x, w.x, s); s = dot2bf(aw[jp].y, w.y, s); s = dot2bf(aw[jp].z, w.z, s); s = dot2bf(aw[jp].w, w.w, s); }
;                 pg[g] = s; }
;             float p8[8], p4[4], p2[2], p1;
;             { const bool hi = (lane & 32) != 0;
; #pragma unroll
;               for (int i = 0; i < 8; ++i) { const float send = hi ? pg[i] : pg[8 + i], keep = hi ? pg[8 + i] : pg[i]; p8[i] = keep + SHX(send, 32); } }
;             { const bool hi = (lane & 16) != 0;
; #pragma unroll
;               for (int i = 0; i < 4; ++i) { const float send = hi ? p8[i] : p8[4 + i], keep = hi ? p8[4 + i] : p8[i]; p4[i] = keep + SHX(send, 16); } }
;             { const bool hi = (lane & 8) != 0;
; #pragma unroll
;               for (int i = 0; i < 2; ++i) { const float send = hi ? p4[i] : p4[2 + i], keep = hi ? p4[2 + i] : p4[i]; p2[i] = keep + SHX(send, 8); } }
;             { const bool hi = (lane & 4) != 0; const float send = hi ? p2[0] : p2[1], keep = hi ? p2[1] : p2[0]; p1 = keep + SHX(send, 4); }
;             p1 += SHX(p1, 2); p1 += SHX(p1, 1);
;             const int src = (((lane >> 3) & 1) << 5) | (((lane >> 2) & 1) << 4) | (((lane >> 1) & 1) << 3) | ((lane & 1) << 2);
;             const float mine = __int_as_float(__builtin_amdgcn_ds_bpermute(src << 2, __float_as_int(p1)));
;             if (lane < 16) { float gv = mine + P.gate_b[layer * 16 + lane]; if ((lane >> 2) & 1) gv = logsigf_(gv); ((float*)(P.ws + WS_GATES))[(size_t)row * 16 + lane] = gv; }
	v_dot2c_f32_bf16_e32 v41, v2, v34
	v_dot2c_f32_bf16_e32 v41, v3, v35
	v_dot2c_f32_bf16_e32 v41, v4, v36
	v_dot2c_f32_bf16_e32 v41, v5, v37
	ds_read_b128 v[34:37], v11 offset:30720
	s_waitcnt lgkmcnt(0)
	v_dot2c_f32_bf16_e32 v42, v6, v34
	v_dot2c_f32_bf16_e32 v42, v7, v35
	v_dot2c_f32_bf16_e32 v42, v8, v36
	v_dot2c_f32_bf16_e32 v42, v9, v37
	ds_read_b128 v[6:9], v11 offset:31744
	s_waitcnt lgkmcnt(0)
	v_dot2c_f32_bf16_e32 v42, v2, v6
	v_dot2c_f32_bf16_e32 v42, v3, v7
	v_dot2c_f32_bf16_e32 v42, v4, v8
	v_mbcnt_lo_u32_b32 v4, -1, 0
	v_cndmask_b32_e32 v2, v10, v30, vcc
	v_mbcnt_hi_u32_b32 v4, -1, v4
	v_dot2c_f32_bf16_e32 v42, v5, v9
	v_lshlrev_b32_e32 v4, 2, v4
	v_xor_b32_e32 v4, 0x80, v4
	ds_bpermute_b32 v2, v4, v2
	v_mbcnt_lo_u32_b32 v5, -1, 0
	v_cndmask_b32_e32 v3, v30, v10, vcc
	v_mbcnt_hi_u32_b32 v5, -1, v5
	v_mbcnt_lo_u32_b32 v6, -1, 0
	s_waitcnt lgkmcnt(0)
	v_add_f32_e32 v2, v3, v2
	v_lshlrev_b32_e32 v5, 2, v5
	v_cndmask_b32_e32 v3, v12, v31, vcc
	v_xor_b32_e32 v5, 0x80, v5
	ds_bpermute_b32 v3, v5, v3
	v_mbcnt_hi_u32_b32 v6, -1, v6
	v_cndmask_b32_e32 v4, v31, v12, vcc
	v_lshlrev_b32_e32 v6, 2, v6
	v_xor_b32_e32 v6, 0x80, v6
	s_waitcnt lgkmcnt(0)
	v_add_f32_e32 v3, v4, v3
	v_cndmask_b32_e32 v4, v13, v33, vcc
	ds_bpermute_b32 v4, v6, v4
	v_mbcnt_lo_u32_b32 v7, -1, 0
	v_cndmask_b32_e32 v5, v33, v13, vcc
	v_mbcnt_hi_u32_b32 v7, -1, v7
	v_mbcnt_lo_u32_b32 v8, -1, 0
	s_waitcnt lgkmcnt(0)
	v_add_f32_e32 v4, v5, v4
	v_lshlrev_b32_e32 v7, 2, v7
	v_cndmask_b32_e32 v5, v14, v38, vcc
	v_xor_b32_e32 v7, 0x80, v7
	ds_bpermute_b32 v5, v7, v5
	v_mbcnt_hi_u32_b32 v8, -1, v8
	v_cndmask_b32_e32 v6, v38, v14, vcc
	v_lshlrev_b32_e32 v8, 2, v8
	v_xor_b32_e32 v8, 0x80, v8
	s_waitcnt lgkmcnt(0)
	v_add_f32_e32 v5, v6, v5
	v_cndmask_b32_e32 v6, v15, v39, vcc
	ds_bpermute_b32 v6, v8, v6
	v_mbcnt_lo_u32_b32 v9, -1, 0
	v_cndmask_b32_e32 v7, v39, v15, vcc
	v_mbcnt_hi_u32_b32 v9, -1, v9
	v_mbcnt_lo_u32_b32 v10, -1, 0
	s_waitcnt lgkmcnt(0)
	v_add_f32_e32 v6, v7, v6
	v_lshlrev_b32_e32 v9, 2, v9
	v_cndmask_b32_e32 v7, v16, v40, vcc
	v_xor_b32_e32 v9, 0x80, v9
	ds_bpermute_b32 v7, v9, v7
	v_mbcnt_hi_u32_b32 v10, -1, v10
	v_cndmask_b32_e32 v8, v40, v16, vcc
	v_lshlrev_b32_e32 v10, 2, v10
	v_xor_b32_e32 v10, 0x80, v10
	s_waitcnt lgkmcnt(0)
	v_add_f32_e32 v7, v8, v7
	v_cndmask_b32_e32 v8, v17, v41, vcc
	ds_bpermute_b32 v8, v10, v8
	v_mbcnt_lo_u32_b32 v11, -1, 0
	v_cndmask_b32_e32 v9, v41, v17, vcc
	v_mbcnt_hi_u32_b32 v11, -1, v11
	v_cndmask_b32_e32 v10, v42, v19, vcc
	v_lshlrev_b32_e32 v11, 2, v11
	s_waitcnt lgkmcnt(0)
	v_add_f32_e32 v8, v9, v8
	v_cndmask_b32_e32 v9, v19, v42, vcc
	v_xor_b32_e32 v11, 0x80, v11
	ds_bpermute_b32 v9, v11, v9
	s_waitcnt lgkmcnt(0)
	v_add_f32_e32 v9, v10, v9
	v_cndmask_b32_e64 v10, v2, v6, s[38:39]
	v_cndmask_b32_e64 v2, v6, v2, s[38:39]
	ds_swizzle_b32 v6, v10 offset:swizzle(SWAP,16)
	s_waitcnt lgkmcnt(0)
	v_add_f32_e32 v2, v2, v6
	v_cndmask_b32_e64 v6, v3, v7, s[38:39]
	ds_swizzle_b32 v6, v6 offset:swizzle(SWAP,16)
	v_cndmask_b32_e64 v3, v7, v3, s[38:39]
	s_waitcnt lgkmcnt(0)
	v_add_f32_e32 v3, v3, v6
	v_cndmask_b32_e64 v6, v4, v8, s[38:39]
	ds_swizzle_b32 v6, v6 offset:swizzle(SWAP,16)
	v_cndmask_b32_e64 v4, v8, v4, s[38:39]
	s_waitcnt lgkmcnt(0)
	v_add_f32_e32 v4, v4, v6
	v_cndmask_b32_e64 v6, v5, v9, s[38:39]
	ds_swizzle_b32 v6, v6 offset:swizzle(SWAP,16)
	v_cndmask_b32_e64 v5, v9, v5, s[38:39]
	s_waitcnt lgkmcnt(0)
	v_add_f32_e32 v5, v5, v6
	v_cndmask_b32_e64 v6, v2, v4, s[40:41]
	v_cndmask_b32_e64 v2, v4, v2, s[40:41]
	ds_swizzle_b32 v4, v6 offset:swizzle(SWAP,8)
	s_waitcnt lgkmcnt(0)
	v_add_f32_e32 v2, v2, v4
	v_cndmask_b32_e64 v4, v3, v5, s[40:41]
	ds_swizzle_b32 v4, v4 offset:swizzle(SWAP,8)
	v_cndmask_b32_e64 v3, v5, v3, s[40:41]
	s_waitcnt lgkmcnt(0)
	v_add_f32_e32 v3, v3, v4
	v_cndmask_b32_e64 v4, v2, v3, s[42:43]
	v_cndmask_b32_e64 v2, v3, v2, s[42:43]
	ds_swizzle_b32 v3, v4 offset:swizzle(SWAP,4)
	s_waitcnt lgkmcnt(0)
	v_add_f32_e32 v2, v2, v3
	ds_swizzle_b32 v3, v2 offset:swizzle(SWAP,2)
	s_waitcnt lgkmcnt(0)
	v_add_f32_e32 v2, v2, v3
	s_waitcnt lgkmcnt(0)
	s_nop 1
	v_add_f32_dpp v2, v2, v2 quad_perm:[1,0,3,2] row_mask:0xf bank_mask:0xf
	ds_bpermute_b32 v2, v32, v2
	s_and_saveexec_b64 s[8:9], s[44:45]
	s_cbranch_execz .LBB0_278
	global_load_dword v3, v[22:23], off
	s_waitcnt vmcnt(0) lgkmcnt(0)
	v_add_f32_e32 v2, v3, v2
	s_and_saveexec_b64 s[18:19], s[46:47]
	s_cbranch_execz .LBB0_277
	s_mov_b32 s4, 0xbfb8aa3b
	v_mul_f32_e64 v3, |v2|, s4
	v_exp_f32_e32 v3, v3
	s_mov_b32 s4, 0x3f317217
	v_max_f32_e32 v2, v2, v2
	v_min_f32_e32 v2, 0, v2
	v_add_f32_e32 v3, 1.0, v3
	v_cmp_gt_f32_e64 s[48:49], s73, v3
	s_nop 1
	v_cndmask_b32_e64 v4, 0, 32, s[48:49]
	v_ldexp_f32 v3, v3, v4
	v_log_f32_e32 v3, v3
	s_nop 0
	v_mul_f32_e32 v4, 0x3f317217, v3
	v_fma_f32 v4, v3, s4, -v4
	v_fmac_f32_e32 v4, 0x3377d1cf, v3
	s_mov_b32 s4, 0x7f800000
	v_fmac_f32_e32 v4, 0x3f317217, v3
	v_cmp_lt_f32_e64 s[50:51], |v3|, s4
	s_nop 1
	v_cndmask_b32_e64 v3, v3, v4, s[50:51]
	v_cndmask_b32_e64 v4, 0, v247, s[48:49]
	v_sub_f32_e32 v3, v3, v4
	v_sub_f32_e32 v2, v2, v3
	s_branch .LBB0_277

; __device__ __forceinline__ float shx32(float v) { return __int_as_float(__builtin_amdgcn_ds_bpermute((olane() ^ 32) << 2, __float_as_int(v))); }
; #define SHX(v, m) (((m) < 32) ? __int_as_float(__builtin_amdgcn_ds_swizzle(__float_as_int(v), ((((m) & 31) << 10) | 0x1f))) : shx32(v))
;     __device__ __forceinline__ void fused(f32x4 (&acc)[2][2][4][2], const Unit& u, int wr, int wc, int fr, int fq, LAS unsigned char* lds, int wid, int lane) const {
;     ...
;         for (int ai = 0; ai < 2; ++ai)
; #pragma unroll
;             for (int m = 0; m < 4; ++m) { float q = 0.f;
; #pragma unroll
;                 for (int bj = 0; bj < 2; ++bj)
; #pragma unroll
;                     for (int n = 0; n < 2; ++n) { const f32x4 x = acc[ai][bj][m][n]; q += (x[0] * x[0] + x[1] * x[1]) + (x[2] * x[2] + x[3] * x[3]); }
;                 q += SHX(q, 16); q += shx32(q);
;                 if (fq == 0) Pp[(ai * 128 + wr * 64 + m * 16 + fr) * 4 + wc] = q; }
.LBB0_902:
	s_or_b64 exec, exec, s[8:9]
	s_waitcnt lgkmcnt(0)
	v_pk_mul_f32 v[4:5], v[118:119], v[118:119]
	v_pk_mul_f32 v[6:7], v[120:121], v[120:121]
	v_pk_mul_f32 v[8:9], v[110:111], v[110:111]
	v_pk_mul_f32 v[10:11], v[112:113], v[112:113]
	v_add_f32_e32 v8, v8, v9
	v_add_f32_e32 v3, v10, v11
	v_add_f32_e32 v6, v6, v7
	v_add_f32_e32 v4, v4, v5
	v_pk_mul_f32 v[12:13], v[158:159], v[158:159]
	v_pk_mul_f32 v[14:15], v[160:161], v[160:161]
	v_add_f32_e32 v3, v8, v3
	v_add_f32_e32 v4, v4, v6
	v_add_f32_e32 v3, v4, v3
	v_add_f32_e32 v4, v14, v15
	v_add_f32_e32 v5, v12, v13
	v_pk_mul_f32 v[16:17], v[168:169], v[168:169]
	v_pk_mul_f32 v[66:67], v[148:149], v[148:149]
	v_add_f32_e32 v4, v5, v4
	v_add_f32_e32 v3, v3, v4
	v_add_f32_e32 v4, v66, v67
	v_add_f32_e32 v5, v16, v17
	v_add_f32_e32 v4, v5, v4
	v_add_f32_e32 v3, v4, v3
	v_mov_b32_e32 v4, v3
	s_nop 1
	v_permlane16_swap_b32 v3, v4
	s_waitcnt lgkmcnt(0)
	v_add_f32_e32 v3, v3, v4
	s_nop 0
	s_nop 0
	v_mov_b32_e32 v4, v3
	s_nop 1
	v_permlane32_swap_b32 v3, v4
	s_and_saveexec_b64 s[8:9], vcc
	v_readlane_b32 s36, v255, 56
	v_readlane_b32 s52, v255, 57
	v_readlane_b32 s71, v255, 58
	s_movk_i32 s63, 0x2440
	s_movk_i32 s62, 0x2000
	s_movk_i32 s61, 0xdff
	s_cbranch_execz .LBB0_904
	s_waitcnt lgkmcnt(0)
	v_add_f32_e32 v3, v3, v4
	ds_write_b32 v2, v3 offset:256
.LBB0_904:
	s_or_b64 exec, exec, s[8:9]
	s_waitcnt lgkmcnt(0)
	v_pk_mul_f32 v[4:5], v[126:127], v[126:127]
	v_pk_mul_f32 v[6:7], v[142:143], v[142:143]
	v_pk_mul_f32 v[8:9], v[146:147], v[146:147]
	v_pk_mul_f32 v[10:11], v[144:145], v[144:145]
	v_add_f32_e32 v8, v8, v9
	v_add_f32_e32 v3, v10, v11
	v_add_f32_e32 v6, v6, v7
	v_add_f32_e32 v4, v4, v5
	v_pk_mul_f32 v[12:13], v[108:109], v[108:109]
	v_pk_mul_f32 v[14:15], v[114:115], v[114:115]
	v_add_f32_e32 v3, v8, v3
	v_add_f32_e32 v4, v4, v6
	v_add_f32_e32 v3, v4, v3
	v_add_f32_e32 v4, v14, v15
	v_add_f32_e32 v5, v12, v13
	v_pk_mul_f32 v[16:17], v[116:117], v[116:117]
	v_pk_mul_f32 v[66:67], v[124:125], v[124:125]
	v_add_f32_e32 v4, v5, v4
	v_add_f32_e32 v3, v3, v4
	v_add_f32_e32 v4, v66, v67
	v_add_f32_e32 v5, v16, v17
	v_add_f32_e32 v4, v5, v4
	v_add_f32_e32 v3, v4, v3
	v_mov_b32_e32 v4, v3
	s_nop 1
	v_permlane16_swap_b32 v3, v4
	s_waitcnt lgkmcnt(0)
	v_add_f32_e32 v3, v3, v4
	s_nop 0
	s_nop 0
	v_mov_b32_e32 v4, v3
	s_nop 1
	v_permlane32_swap_b32 v3, v4
	s_and_saveexec_b64 s[8:9], vcc
	s_cbranch_execz .LBB0_906
	s_waitcnt lgkmcnt(0)
	v_add_f32_e32 v3, v3, v4
	ds_write_b32 v2, v3 offset:512
.LBB0_906:
	s_or_b64 exec, exec, s[8:9]
	s_waitcnt lgkmcnt(0)
	v_pk_mul_f32 v[4:5], v[100:101], v[100:101]
	v_pk_mul_f32 v[6:7], v[102:103], v[102:103]
	v_pk_mul_f32 v[8:9], v[104:105], v[104:105]
	v_pk_mul_f32 v[10:11], v[106:107], v[106:107]
	v_add_f32_e32 v8, v8, v9
	v_add_f32_e32 v3, v10, v11
	v_add_f32_e32 v6, v6, v7
	v_add_f32_e32 v4, v4, v5
	v_pk_mul_f32 v[12:13], v[92:93], v[92:93]
	v_pk_mul_f32 v[14:15], v[94:95], v[94:95]
	v_add_f32_e32 v3, v8, v3
	v_add_f32_e32 v4, v4, v6
	v_add_f32_e32 v3, v4, v3
	v_add_f32_e32 v4, v14, v15
	v_add_f32_e32 v5, v12, v13
	v_pk_mul_f32 v[16:17], v[96:97], v[96:97]
	v_pk_mul_f32 v[66:67], v[98:99], v[98:99]
	v_add_f32_e32 v4, v5, v4
	v_add_f32_e32 v3, v3, v4
	v_add_f32_e32 v4, v66, v67
	v_add_f32_e32 v5, v16, v17
	v_add_f32_e32 v4, v5, v4
	v_add_f32_e32 v3, v4, v3
	v_mov_b32_e32 v4, v3
	s_nop 1
	v_permlane16_swap_b32 v3, v4
	s_waitcnt lgkmcnt(0)
	v_add_f32_e32 v3, v3, v4
	s_nop 0
	s_nop 0
	v_mov_b32_e32 v4, v3
	s_nop 1
	v_permlane32_swap_b32 v3, v4
	s_and_saveexec_b64 s[8:9], vcc
	s_cbranch_execz .LBB0_908
	s_waitcnt lgkmcnt(0)
	v_add_f32_e32 v3, v3, v4
	ds_write_b32 v2, v3 offset:768
; __device__ __forceinline__ float shx32(float v) { return __int_as_float(__builtin_amdgcn_ds_bpermute((olane() ^ 32) << 2, __float_as_int(v))); }
; #define SHX(v, m) (((m) < 32) ? __int_as_float(__builtin_amdgcn_ds_swizzle(__float_as_int(v), ((((m) & 31) << 10) | 0x1f))) : shx32(v))
;     __device__ __forceinline__ void fused(f32x4 (&acc)[2][2][4][2], const Unit& u, int wr, int wc, int fr, int fq, LAS unsigned char* lds, int wid, int lane) const {
;     ...
;         for (int ai = 0; ai < 2; ++ai)
; #pragma unroll
;             for (int m = 0; m < 4; ++m) { float q = 0.f;
; #pragma unroll
;                 for (int bj = 0; bj < 2; ++bj)
; #pragma unroll
;                     for (int n = 0; n < 2; ++n) { const f32x4 x = acc[ai][bj][m][n]; q += (x[0] * x[0] + x[1] * x[1]) + (x[2] * x[2] + x[3] * x[3]); }
;                 q += SHX(q, 16); q += shx32(q);
;                 if (fq == 0) Pp[(ai * 128 + wr * 64 + m * 16 + fr) * 4 + wc] = q; }
.LBB0_908:
	s_or_b64 exec, exec, s[8:9]
	s_waitcnt lgkmcnt(0)
	v_pk_mul_f32 v[4:5], v[132:133], v[132:133]
	v_pk_mul_f32 v[6:7], v[134:135], v[134:135]
	v_pk_mul_f32 v[8:9], v[136:137], v[136:137]
	v_pk_mul_f32 v[10:11], v[138:139], v[138:139]
	v_add_f32_e32 v8, v8, v9
	v_add_f32_e32 v3, v10, v11
	v_add_f32_e32 v6, v6, v7
	v_add_f32_e32 v4, v4, v5
	v_pk_mul_f32 v[12:13], v[74:75], v[74:75]
	v_pk_mul_f32 v[14:15], v[76:77], v[76:77]
	v_add_f32_e32 v3, v8, v3
	v_add_f32_e32 v4, v4, v6
	v_add_f32_e32 v3, v4, v3
	v_add_f32_e32 v4, v14, v15
	v_add_f32_e32 v5, v12, v13
	v_pk_mul_f32 v[16:17], v[78:79], v[78:79]
	v_pk_mul_f32 v[66:67], v[80:81], v[80:81]
	v_add_f32_e32 v4, v5, v4
	v_add_f32_e32 v3, v3, v4
	v_add_f32_e32 v4, v66, v67
	v_add_f32_e32 v5, v16, v17
	v_add_f32_e32 v4, v5, v4
	v_add_f32_e32 v3, v4, v3
	v_mov_b32_e32 v4, v3
	s_nop 1
	v_permlane16_swap_b32 v3, v4
	s_waitcnt lgkmcnt(0)
	v_add_f32_e32 v3, v3, v4
	s_nop 0
	s_nop 0
	v_mov_b32_e32 v4, v3
	s_nop 1
	v_permlane32_swap_b32 v3, v4
	s_and_saveexec_b64 s[8:9], vcc
	s_cbranch_execz .LBB0_910
	s_waitcnt lgkmcnt(0)
	v_add_f32_e32 v3, v3, v4
	ds_write_b32 v2, v3 offset:2048
.LBB0_910:
	s_or_b64 exec, exec, s[8:9]
	s_waitcnt lgkmcnt(0)
	v_pk_mul_f32 v[4:5], v[58:59], v[58:59]
	v_pk_mul_f32 v[6:7], v[60:61], v[60:61]
	v_pk_mul_f32 v[8:9], v[62:63], v[62:63]
	v_pk_mul_f32 v[10:11], v[64:65], v[64:65]
	v_add_f32_e32 v8, v8, v9
	v_add_f32_e32 v3, v10, v11
	v_add_f32_e32 v6, v6, v7
	v_add_f32_e32 v4, v4, v5
	v_pk_mul_f32 v[12:13], v[50:51], v[50:51]
	v_pk_mul_f32 v[14:15], v[52:53], v[52:53]
	v_add_f32_e32 v3, v8, v3
	v_add_f32_e32 v4, v4, v6
	v_add_f32_e32 v3, v4, v3
	v_add_f32_e32 v4, v14, v15
	v_add_f32_e32 v5, v12, v13
	v_pk_mul_f32 v[16:17], v[54:55], v[54:55]
	v_pk_mul_f32 v[66:67], v[56:57], v[56:57]
	v_add_f32_e32 v4, v5, v4
	v_add_f32_e32 v3, v3, v4
	v_add_f32_e32 v4, v66, v67
	v_add_f32_e32 v5, v16, v17
	v_add_f32_e32 v4, v5, v4
	v_add_f32_e32 v3, v4, v3
	v_mov_b32_e32 v4, v3
	s_nop 1
	v_permlane16_swap_b32 v3, v4
	s_waitcnt lgkmcnt(0)
	v_add_f32_e32 v3, v3, v4
	s_nop 0
	s_nop 0
	v_mov_b32_e32 v4, v3
	s_nop 1
	v_permlane32_swap_b32 v3, v4
	s_and_saveexec_b64 s[8:9], vcc
	s_cbranch_execz .LBB0_912
	s_waitcnt lgkmcnt(0)
	v_add_f32_e32 v3, v3, v4
	ds_write_b32 v2, v3 offset:2304
.LBB0_912:
	s_or_b64 exec, exec, s[8:9]
	s_waitcnt lgkmcnt(0)
	v_pk_mul_f32 v[4:5], v[42:43], v[42:43]
	v_pk_mul_f32 v[6:7], v[44:45], v[44:45]
	v_pk_mul_f32 v[8:9], v[46:47], v[46:47]
	v_pk_mul_f32 v[10:11], v[48:49], v[48:49]
	v_add_f32_e32 v8, v8, v9
	v_add_f32_e32 v3, v10, v11
	v_add_f32_e32 v6, v6, v7
	v_add_f32_e32 v4, v4, v5
	v_pk_mul_f32 v[12:13], v[34:35], v[34:35]
	v_pk_mul_f32 v[14:15], v[36:37], v[36:37]
	v_add_f32_e32 v3, v8, v3
	v_add_f32_e32 v4, v4, v6
	v_add_f32_e32 v3, v4, v3
	v_add_f32_e32 v4, v14, v15
	v_add_f32_e32 v5, v12, v13
	v_pk_mul_f32 v[16:17], v[38:39], v[38:39]
	v_pk_mul_f32 v[66:67], v[40:41], v[40:41]
	v_add_f32_e32 v4, v5, v4
	v_add_f32_e32 v3, v3, v4
	v_add_f32_e32 v4, v66, v67
	v_add_f32_e32 v5, v16, v17
	v_add_f32_e32 v4, v5, v4
	v_add_f32_e32 v3, v4, v3
	v_mov_b32_e32 v4, v3
	s_nop 1
	v_permlane16_swap_b32 v3, v4
	s_waitcnt lgkmcnt(0)
	v_add_f32_e32 v3, v3, v4
	s_nop 0
	s_nop 0
	v_mov_b32_e32 v4, v3
	s_nop 1
	v_permlane32_swap_b32 v3, v4
	s_and_saveexec_b64 s[8:9], vcc
	s_cbranch_execz .LBB0_914
	s_waitcnt lgkmcnt(0)
	v_add_f32_e32 v3, v3, v4
	ds_write_b32 v2, v3 offset:2560
.LBB0_914:
	s_or_b64 exec, exec, s[8:9]
	s_waitcnt lgkmcnt(0)
	v_pk_mul_f32 v[4:5], v[26:27], v[26:27]
	v_pk_mul_f32 v[6:7], v[28:29], v[28:29]
	v_pk_mul_f32 v[8:9], v[30:31], v[30:31]
	v_pk_mul_f32 v[10:11], v[32:33], v[32:33]
	v_add_f32_e32 v8, v8, v9
	v_add_f32_e32 v3, v10, v11
	v_add_f32_e32 v6, v6, v7
	v_add_f32_e32 v4, v4, v5
	v_pk_mul_f32 v[12:13], v[18:19], v[18:19]
	v_pk_mul_f32 v[14:15], v[20:21], v[20:21]
	v_add_f32_e32 v3, v8, v3
	v_add_f32_e32 v4, v4, v6
	v_add_f32_e32 v3, v4, v3
	v_add_f32_e32 v4, v14, v15
	v_add_f32_e32 v5, v12, v13
	v_pk_mul_f32 v[16:17], v[22:23], v[22:23]
	v_pk_mul_f32 v[66:67], v[24:25], v[24:25]
	v_add_f32_e32 v4, v5, v4
	v_add_f32_e32 v3, v3, v4
	v_add_f32_e32 v4, v66, v67
	v_add_f32_e32 v5, v16, v17
	v_add_f32_e32 v4, v5, v4
	v_add_f32_e32 v3, v4, v3
	v_mov_b32_e32 v4, v3
	s_nop 1
	v_permlane16_swap_b32 v3, v4
	s_waitcnt lgkmcnt(0)
	v_add_f32_e32 v3, v3, v4
	s_nop 0
	s_nop 0
	v_mov_b32_e32 v4, v3
	s_nop 1
	v_permlane32_swap_b32 v3, v4
	s_and_saveexec_b64 s[8:9], vcc
	s_cbranch_execz .LBB0_916
	s_waitcnt lgkmcnt(0)
	v_add_f32_e32 v3, v3, v4
	ds_write_b32 v2, v3 offset:2816

; __device__ __forceinline__ unsigned pk2(float lo, float hi) { unsigned r; asm("v_cvt_pk_bf16_f32 %0, %1, %2" : "=v"(r) : "v"(lo), "v"(hi)); return r; }
; __device__ __forceinline__ float bflo(unsigned w) { return __uint_as_float(w << 16); }
; __device__ __forceinline__ float bfhi(unsigned w) { return __uint_as_float(w & 0xffff0000u); }
; __device__ __forceinline__ void phase_rowpass2(const Ptrs& P, int layer, int tid_, int vcu, int G) {
;     ...
;     for (int row = gw; row < T; row += NGW) {
;         f32x4 v[4]; float ss = 0.f;
; #pragma unroll
;         for (int jp = 0; jp < 2; ++jp) { const v4u hw = ((const v4u*)(H + (size_t)row * D))[lane + 64 * jp];
;             v[2 * jp] = (f32x4){bflo(hw.x), bfhi(hw.x), bflo(hw.y), bfhi(hw.y)}; v[2 * jp + 1] = (f32x4){bflo(hw.z), bfhi(hw.z), bflo(hw.w), bfhi(hw.w)}; }
; #pragma unroll
;         for (int j = 0; j < 4; ++j) ss += v[j][0] * v[j][0] + v[j][1] * v[j][1] + v[j][2] * v[j][2] + v[j][3] * v[j][3];
;         const float rstd = rsqrtf(wave_sum(ss) * (1.f / D) + EPS);
;         bf16* A = (bf16*)(P.ws + WS_XM) + (size_t)row * D;
; #pragma unroll
;         for (int jp = 0; jp < 2; ++jp) { float x[8];
; #pragma unroll
;             for (int h = 0; h < 2; ++h) { const f32x4 g = ((const f32x4*)g2)[F4(2 * jp + h)];
; #pragma unroll
;                 for (int i = 0; i < 4; ++i) x[4 * h + i] = v[2 * jp + h][i] * rstd * g[i]; }
;             v4u w; w.x = pk2(x[0], x[1]); w.y = pk2(x[2], x[3]); w.z = pk2(x[4], x[5]); w.w = pk2(x[6], x[7]); ((v4u*)A)[lane + 64 * jp] = w;
;             v2u w8; w8.x = (unsigned)__builtin_amdgcn_cvt_pk_fp8_f32(x[2] * SX8, x[3] * SX8, __builtin_amdgcn_cvt_pk_fp8_f32(x[0] * SX8, x[1] * SX8, 0, false), true);
;             w8.y = (unsigned)__builtin_amdgcn_cvt_pk_fp8_f32(x[6] * SX8, x[7] * SX8, __builtin_amdgcn_cvt_pk_fp8_f32(x[4] * SX8, x[5] * SX8, 0, false), true);
;             ((v2u*)(P.ws + WS_XM8 + (size_t)row * D))[lane + 64 * jp] = w8; }
;     }
.LBB0_985:
	v_lshl_add_u64 v[28:29], s[6:7], 0, v[6:7]
	v_add_co_u32_e32 v12, vcc, 0x34600000, v28
	s_mov_b32 s4, 0x6a200000
	s_nop 0
	v_addc_co_u32_e32 v13, vcc, 0, v29, vcc
	global_load_dwordx4 v[8:11], v[12:13], off
	global_load_dwordx4 v[16:19], v[12:13], off offset:1024
	v_add_u32_e32 v1, s74, v1
	v_lshl_add_u64 v[6:7], v[6:7], 0, s[94:95]
	s_waitcnt vmcnt(1)
	v_and_b32_e32 v31, 0xffff0000, v10
	v_and_b32_e32 v30, 0xffff0000, v8
	v_lshlrev_b32_e32 v21, 16, v10
	v_lshlrev_b32_e32 v20, 16, v8
	v_lshlrev_b32_e32 v32, 16, v9
	v_and_b32_e32 v34, 0xffff0000, v9
	v_pk_mul_f32 v[8:9], v[30:31], v[30:31]
	v_lshlrev_b32_e32 v33, 16, v11
	v_pk_fma_f32 v[8:9], v[20:21], v[20:21], v[8:9]
	v_and_b32_e32 v35, 0xffff0000, v11
	v_pk_fma_f32 v[8:9], v[32:33], v[32:33], v[8:9]
	s_waitcnt vmcnt(0)
	v_lshlrev_b32_e32 v15, 16, v16
	v_pk_fma_f32 v[22:23], v[34:35], v[34:35], v[8:9]
	v_and_b32_e32 v9, 0xffff0000, v16
	v_and_b32_e32 v8, 0xffff0000, v18
	v_lshlrev_b32_e32 v14, 16, v18
	v_lshlrev_b32_e32 v13, 16, v17
	v_and_b32_e32 v11, 0xffff0000, v17
	v_pk_mul_f32 v[16:17], v[8:9], v[8:9]
	v_lshlrev_b32_e32 v12, 16, v19
	v_pk_fma_f32 v[16:17], v[14:15], v[14:15], v[16:17]
	v_and_b32_e32 v10, 0xffff0000, v19
	v_pk_fma_f32 v[16:17], v[12:13], v[12:13], v[16:17]
	v_add_f32_e32 v18, v22, v23
	v_pk_fma_f32 v[16:17], v[10:11], v[10:11], v[16:17]
	s_nop 0
	v_add_f32_e32 v17, v18, v17
	v_add_f32_e32 v16, v16, v17
	s_waitcnt lgkmcnt(0)
	s_nop 1
	v_add_f32_dpp v16, v16, v16 quad_perm:[1,0,3,2] row_mask:0xf bank_mask:0xf
	s_waitcnt lgkmcnt(0)
	s_nop 1
	v_add_f32_dpp v16, v16, v16 quad_perm:[2,3,0,1] row_mask:0xf bank_mask:0xf
	s_waitcnt lgkmcnt(0)
	s_nop 1
	v_add_f32_dpp v16, v16, v16 row_half_mirror row_mask:0xf bank_mask:0xf
	s_waitcnt lgkmcnt(0)
	s_nop 1
	v_add_f32_dpp v16, v16, v16 row_mirror row_mask:0xf bank_mask:0xf
	v_mov_b32_e32 v17, v16
	s_nop 1
	v_permlane16_swap_b32 v16, v17
	s_waitcnt lgkmcnt(0)
	v_add_f32_e32 v16, v16, v17
	s_nop 0
	s_nop 0
	v_mov_b32_e32 v17, v16
	s_nop 1
	v_permlane32_swap_b32 v16, v17
	s_waitcnt lgkmcnt(0)
	v_add_f32_e32 v16, v16, v17
	v_fmamk_f32 v16, v16, 0x3a800000, v196
	v_cmp_gt_f32_e32 vcc, s73, v16
	v_mul_f32_e32 v17, 0x4b800000, v16
	s_nop 0
	v_cndmask_b32_e32 v16, v16, v17, vcc
	v_rsq_f32_e32 v16, v16
	s_nop 0
	v_mul_f32_e32 v17, 0x45800000, v16
	v_cndmask_b32_e32 v22, v16, v17, vcc
	global_load_dwordx4 v[16:19], v[2:3], off offset:16
	global_load_dwordx4 v[24:27], v[2:3], off
	v_mul_f32_e32 v20, v22, v20
	v_mul_f32_e32 v9, v22, v9
	v_mul_f32_e32 v8, v22, v8
	v_mul_f32_e32 v15, v22, v15
	s_waitcnt vmcnt(0)
	v_mul_f32_e32 v23, v24, v20
	v_mul_f32_e32 v20, v22, v30
	v_mul_f32_e32 v24, v25, v20
	v_mul_f32_e32 v20, v22, v32
	v_mul_f32_e32 v25, v26, v20
	v_mul_f32_e32 v20, v22, v34
	v_mul_f32_e32 v26, v27, v20
	v_mul_f32_e32 v20, v22, v21
	v_mul_f32_e32 v27, v16, v20
	v_mul_f32_e32 v16, v22, v31
	v_mul_f32_e32 v30, v17, v16
	v_mul_f32_e32 v16, v22, v33
	v_mul_f32_e32 v31, v18, v16
	v_mul_f32_e32 v16, v22, v35
	v_mul_f32_e32 v32, v19, v16
	v_add_co_u32_e32 v16, vcc, s25, v28
	v_cvt_pk_bf16_f32 v20, v27, v30
	v_cvt_pk_bf16_f32 v21, v31, v32
	v_cvt_pk_bf16_f32 v18, v23, v24
	v_cvt_pk_bf16_f32 v19, v25, v26
	s_nop 1
	v_addc_co_u32_e32 v17, vcc, 0, v29, vcc
	global_store_dwordx4 v[16:17], v[18:21], off
	s_nop 1
	v_mul_f32_e32 v21, 0x41000000, v23
	v_mul_f32_e32 v23, 0x41000000, v24
	v_mov_b32_e32 v20, v163
	v_cvt_pk_fp8_f32 v20, v21, v23
	v_mul_f32_e32 v23, 0x41000000, v27
	v_mul_f32_e32 v24, 0x41000000, v30
	v_mov_b32_e32 v21, v163
	v_cvt_pk_fp8_f32 v21, v23, v24
	v_mul_f32_e32 v18, 0x41000000, v25
	v_mul_f32_e32 v19, 0x41000000, v26
	v_cvt_pk_fp8_f32 v20, v18, v19 op_sel:[0,0,1]
	v_mul_f32_e32 v18, 0x41000000, v31
	v_mul_f32_e32 v19, 0x41000000, v32
	v_cvt_pk_fp8_f32 v21, v18, v19 op_sel:[0,0,1]
	v_lshl_add_u64 v[18:19], s[6:7], 0, v[4:5]
	v_add_co_u32_e32 v18, vcc, s4, v18
	v_lshl_add_u64 v[4:5], v[4:5], 0, s[10:11]
	s_nop 0
	v_addc_co_u32_e32 v19, vcc, 0, v19, vcc
	global_store_dwordx2 v[18:19], v[20:21], off
	global_load_dwordx4 v[24:27], v[2:3], off offset:2064
	global_load_dwordx4 v[28:31], v[2:3], off offset:2048
	v_cmp_lt_i32_e32 vcc, s9, v1
	s_or_b64 s[12:13], vcc, s[12:13]
	s_waitcnt vmcnt(1)
	v_mul_f32_e32 v23, v25, v8
	s_waitcnt vmcnt(0)
	v_mul_f32_e32 v20, v29, v9
	v_mul_f32_e32 v9, v22, v13
	v_mul_f32_e32 v13, v30, v9
	v_mul_f32_e32 v9, v22, v11
	v_mul_f32_e32 v8, v22, v12
	v_mul_f32_e32 v21, v31, v9
	v_mul_f32_e32 v9, v22, v14
	v_mul_f32_e32 v12, v26, v8
	v_mul_f32_e32 v8, v22, v10
	v_mul_f32_e32 v15, v28, v15
	v_mul_f32_e32 v14, v24, v9
	v_mul_f32_e32 v22, v27, v8
	v_cvt_pk_bf16_f32 v8, v15, v20
	v_cvt_pk_bf16_f32 v9, v13, v21
	v_cvt_pk_bf16_f32 v11, v12, v22
	v_cvt_pk_bf16_f32 v10, v14, v23
	global_store_dwordx4 v[16:17], v[8:11], off offset:1024
	s_nop 1
	v_mul_f32_e32 v9, 0x41000000, v13
	v_mul_f32_e32 v11, 0x41000000, v15
	v_mul_f32_e32 v13, 0x41000000, v20
	v_mov_b32_e32 v8, v163
	v_cvt_pk_fp8_f32 v8, v11, v13
	v_mul_f32_e32 v10, 0x41000000, v21
	v_mul_f32_e32 v13, 0x41000000, v23
	v_mul_f32_e32 v11, 0x41000000, v22
	v_cvt_pk_fp8_f32 v8, v9, v10 op_sel:[0,0,1]
	v_mul_f32_e32 v10, 0x41000000, v12
	v_mul_f32_e32 v12, 0x41000000, v14
	v_mov_b32_e32 v9, v163
	v_cvt_pk_fp8_f32 v9, v12, v13
	v_cvt_pk_fp8_f32 v9, v10, v11 op_sel:[0,0,1]
	global_store_dwordx2 v[18:19], v[8:9], off offset:512
	s_andn2_b64 exec, exec, s[12:13]
	s_cbranch_execnz .LBB0_985

; __device__ __forceinline__ float bflo(unsigned w) { return __uint_as_float(w << 16); }
; __device__ __forceinline__ float bfhi(unsigned w) { return __uint_as_float(w & 0xffff0000u); }
; #define SHX(v, m) (((m) < 32) ? __int_as_float(__builtin_amdgcn_ds_swizzle(__float_as_int(v), ((((m) & 31) << 10) | 0x1f))) : shx32(v))
; __device__ __forceinline__ float wave_sum(float v) {
;     v += SHX(v, 1); v += SHX(v, 2); v += SHX(v, 4); v += SHX(v, 8); v += SHX(v, 16); v += SHX(v, 32);
;     return v;
; template <int MODE>
; __device__ __forceinline__ void phase_rowpass1(const Ptrs& P, LAS unsigned char* lds, int layer, int tid_, int vcu, int G) {
;     ...
;             f32x4 e[4]; float ss = 0.f;
; #pragma unroll
;             for (int jp = 0; jp < 2; ++jp) { const v4u hw = ((const v4u*)(H + (size_t)row * D))[lane + 64 * jp]; const v4u w = __builtin_nontemporal_load((const v4u*)(GE + (size_t)row * D) + lane + 64 * jp);
;                 v[2 * jp] = (f32x4){bflo(hw.x), bfhi(hw.x), bflo(hw.y), bfhi(hw.y)}; v[2 * jp + 1] = (f32x4){bflo(hw.z), bfhi(hw.z), bflo(hw.w), bfhi(hw.w)};
;                 e[2 * jp] = (f32x4){bflo(w.x), bfhi(w.x), bflo(w.y), bfhi(w.y)}; e[2 * jp + 1] = (f32x4){bflo(w.z), bfhi(w.z), bflo(w.w), bfhi(w.w)}; }
; #pragma unroll
;             for (int j = 0; j < 4; ++j) ss += e[j][0] * e[j][0] + e[j][1] * e[j][1] + e[j][2] * e[j][2] + e[j][3] * e[j][3];
;             const float r = rsqrtf(wave_sum(ss) * (1.f / D) + EPS);
; #pragma unroll
;             for (int j = 0; j < 4; ++j) { const f32x4 g = ((const f32x4*)pg)[F4(j)]; v[j] = v[j] + e[j] * r * g; }
.LBB0_1574:
	v_add_co_u32_e32 v18, vcc, 0x31400000, v14
	global_load_dwordx4 v[0:3], v[14:15], off
	global_load_dwordx4 v[4:7], v[14:15], off offset:1024
	v_addc_co_u32_e32 v19, vcc, 0, v15, vcc
	global_load_dwordx4 v[22:25], v[18:19], off nt
	global_load_dwordx4 v[26:29], v[18:19], off offset:1024 nt
	v_mbcnt_lo_u32_b32 v18, -1, 0
	v_add_u32_e32 v20, s74, v20
	v_mbcnt_hi_u32_b32 v18, -1, v18
	global_load_dwordx4 v[30:33], v[8:9], off offset:16
	global_load_dwordx4 v[34:37], v[8:9], off
	global_load_dwordx4 v[38:41], v[10:11], off offset:16
	global_load_dwordx4 v[42:45], v[10:11], off
	v_mbcnt_lo_u32_b32 v19, -1, 0
	v_lshlrev_b32_e32 v18, 2, v18
	v_mbcnt_hi_u32_b32 v19, -1, v19
	global_load_dwordx4 v[46:49], v[12:13], off offset:16
	global_load_dwordx4 v[50:53], v[12:13], off
	global_load_dwordx4 v[54:57], v[12:13], off offset:2064
	global_load_dwordx4 v[58:61], v[12:13], off offset:2048
	v_xor_b32_e32 v88, 0x80, v18
	v_cmp_lt_i32_e32 vcc, s3, v20
	s_or_b64 s[0:1], vcc, s[0:1]
	v_lshlrev_b32_e32 v18, 2, v19
	v_xor_b32_e32 v89, 0x80, v18
	v_lshl_add_u64 v[14:15], v[14:15], 0, s[94:95]
	s_waitcnt vmcnt(11)
	v_lshlrev_b32_e32 v18, 16, v0
	v_and_b32_e32 v19, 0xffff0000, v0
	v_lshlrev_b32_e32 v62, 16, v2
	s_waitcnt vmcnt(9)
	v_and_b32_e32 v71, 0xffff0000, v24
	v_and_b32_e32 v70, 0xffff0000, v22
	v_lshlrev_b32_e32 v69, 16, v24
	v_lshlrev_b32_e32 v68, 16, v22
	v_lshlrev_b32_e32 v72, 16, v23
	v_and_b32_e32 v24, 0xffff0000, v23
	s_waitcnt vmcnt(8)
	v_lshlrev_b32_e32 v23, 16, v26
	v_lshlrev_b32_e32 v22, 16, v28
	v_and_b32_e32 v75, 0xffff0000, v26
	v_and_b32_e32 v74, 0xffff0000, v28
	v_lshlrev_b32_e32 v76, 16, v29
	v_and_b32_e32 v26, 0xffff0000, v29
	v_pk_mul_f32 v[28:29], v[70:71], v[70:71]
	v_lshlrev_b32_e32 v73, 16, v25
	v_pk_mul_f32 v[78:79], v[74:75], v[74:75]
	v_pk_fma_f32 v[28:29], v[68:69], v[68:69], v[28:29]
	v_and_b32_e32 v25, 0xffff0000, v25
	v_lshlrev_b32_e32 v77, 16, v27
	v_mov_b32_e32 v80, v68
	v_mov_b32_e32 v81, v70
	v_mov_b32_e32 v70, v69
	v_pk_fma_f32 v[68:69], v[22:23], v[22:23], v[78:79]
	v_pk_fma_f32 v[28:29], v[72:73], v[72:73], v[28:29]
	v_and_b32_e32 v27, 0xffff0000, v27
	v_pk_fma_f32 v[68:69], v[76:77], v[76:77], v[68:69]
	v_pk_fma_f32 v[28:29], v[24:25], v[24:25], v[28:29]
	v_mov_b32_e32 v86, v77
	v_mov_b32_e32 v87, v27
	v_mov_b32_e32 v77, v26
	v_pk_fma_f32 v[26:27], v[26:27], v[26:27], v[68:69]
	v_add_f32_e32 v28, v28, v29
	v_add_f32_e32 v27, v28, v27
	v_add_f32_e32 v26, v26, v27
	v_mov_b32_e32 v83, v24
	v_mov_b32_e32 v24, v73
	v_and_b32_e32 v63, 0xffff0000, v2
	v_lshlrev_b32_e32 v2, 16, v3
	s_waitcnt lgkmcnt(0)
	s_nop 1
	v_add_f32_dpp v26, v26, v26 quad_perm:[1,0,3,2] row_mask:0xf bank_mask:0xf
	v_and_b32_e32 v3, 0xffff0000, v3
	v_mov_b32_e32 v84, v23
	v_mov_b32_e32 v85, v75
	v_mov_b32_e32 v23, v74
	s_waitcnt lgkmcnt(0)
	s_nop 1
	v_add_f32_dpp v26, v26, v26 quad_perm:[2,3,0,1] row_mask:0xf bank_mask:0xf
	v_lshlrev_b32_e32 v64, 16, v4
	v_and_b32_e32 v65, 0xffff0000, v4
	v_lshlrev_b32_e32 v66, 16, v6
	v_and_b32_e32 v67, 0xffff0000, v6
	s_waitcnt lgkmcnt(0)
	s_nop 1
	v_add_f32_dpp v26, v26, v26 row_half_mirror row_mask:0xf bank_mask:0xf
	v_mov_b32_e32 v82, v72
	v_lshlrev_b32_e32 v0, 16, v1
	v_and_b32_e32 v1, 0xffff0000, v1
	v_lshlrev_b32_e32 v6, 16, v7
	s_waitcnt lgkmcnt(0)
	s_nop 1
	v_add_f32_dpp v26, v26, v26 row_mirror row_mask:0xf bank_mask:0xf
	ds_swizzle_b32 v27, v26 offset:swizzle(SWAP,16)
	v_and_b32_e32 v7, 0xffff0000, v7
	v_lshlrev_b32_e32 v4, 16, v5
	v_and_b32_e32 v5, 0xffff0000, v5
	s_waitcnt lgkmcnt(0)
	v_add_f32_e32 v26, v26, v27
	ds_bpermute_b32 v27, v88, v26
	s_waitcnt lgkmcnt(0)
; __device__ __forceinline__ unsigned pk2(float lo, float hi) { unsigned r; asm("v_cvt_pk_bf16_f32 %0, %1, %2" : "=v"(r) : "v"(lo), "v"(hi)); return r; }
; #define SHX(v, m) (((m) < 32) ? __int_as_float(__builtin_amdgcn_ds_swizzle(__float_as_int(v), ((((m) & 31) << 10) | 0x1f))) : shx32(v))
; __device__ __forceinline__ float wave_sum(float v) {
;     v += SHX(v, 1); v += SHX(v, 2); v += SHX(v, 4); v += SHX(v, 8); v += SHX(v, 16); v += SHX(v, 32);
;     return v;
; template <int MODE>
; __device__ __forceinline__ void phase_rowpass1(const Ptrs& P, LAS unsigned char* lds, int layer, int tid_, int vcu, int G) {
;     ...
;             const float r = rsqrtf(wave_sum(ss) * (1.f / D) + EPS);
; #pragma unroll
;             for (int j = 0; j < 4; ++j) { const f32x4 g = ((const f32x4*)pg)[F4(j)]; v[j] = v[j] + e[j] * r * g; }
;         }
;         if (MODE != 2) {
; #pragma unroll
;             for (int jp = 0; jp < 2; ++jp) { v4u hw; hw.x = pk2(v[2 * jp][0], v[2 * jp][1]); hw.y = pk2(v[2 * jp][2], v[2 * jp][3]); hw.z = pk2(v[2 * jp + 1][0], v[2 * jp + 1][1]); hw.w = pk2(v[2 * jp + 1][2], v[2 * jp + 1][3]);
;                 ((v4u*)(H + (size_t)row * D))[lane + 64 * jp] = hw; }
;         }
;         float ss = 0.f;
; #pragma unroll
;         for (int j = 0; j < 4; ++j) ss += v[j][0] * v[j][0] + v[j][1] * v[j][1] + v[j][2] * v[j][2] + v[j][3] * v[j][3];
;         const float rstd = rsqrtf(wave_sum(ss) * (1.f / D) + EPS);
; #pragma unroll
;         for (int j = 0; j < 4; ++j) { const f32x4 g = ((const f32x4*)g1)[F4(j)]; v[j] = v[j] * rstd * g; }
;         if (MODE == 2) {
; #pragma unroll
;             for (int j = 0; j < 4; ++j) ((f32x4*)(P.out + (size_t)row * D))[F4(j)] = v[j];
	v_add_f32_e32 v26, v26, v27
	v_fmamk_f32 v26, v26, 0x3a800000, v21
	v_mul_f32_e32 v27, 0x4b800000, v26
	v_cmp_gt_f32_e32 vcc, s2, v26
	s_nop 1
	v_cndmask_b32_e32 v26, v26, v27, vcc
	v_rsq_f32_e32 v26, v26
	s_nop 0
	v_mul_f32_e32 v27, 0x45800000, v26
	v_cndmask_b32_e32 v26, v26, v27, vcc
	v_pk_mul_f32 v[28:29], v[80:81], v[26:27] op_sel_hi:[1,0]
	v_pk_mul_f32 v[70:71], v[70:71], v[26:27] op_sel_hi:[1,0]
	v_pk_mul_f32 v[24:25], v[24:25], v[26:27] op_sel_hi:[1,0]
	v_pk_mul_f32 v[72:73], v[84:85], v[26:27] op_sel_hi:[1,0]
	v_pk_mul_f32 v[22:23], v[22:23], v[26:27] op_sel_hi:[1,0]
	s_waitcnt vmcnt(6)
	v_pk_fma_f32 v[18:19], v[34:35], v[28:29], v[18:19]
	v_pk_fma_f32 v[2:3], v[32:33], v[24:25], v[2:3]
	v_pk_fma_f32 v[24:25], v[30:31], v[70:71], v[62:63]
	v_pk_mul_f32 v[68:69], v[82:83], v[26:27] op_sel_hi:[1,0]
	v_pk_mul_f32 v[74:75], v[86:87], v[26:27] op_sel_hi:[1,0]
	v_pk_mul_f32 v[26:27], v[76:77], v[26:27] op_sel_hi:[1,0]
	s_waitcnt vmcnt(4)
	v_pk_fma_f32 v[28:29], v[42:43], v[72:73], v[64:65]
	v_pk_fma_f32 v[22:23], v[38:39], v[22:23], v[66:67]
	v_mov_b32_e32 v30, v19
	v_mov_b32_e32 v31, v25
	v_pk_fma_f32 v[0:1], v[36:37], v[68:69], v[0:1]
	v_pk_fma_f32 v[6:7], v[40:41], v[26:27], v[6:7]
	v_mov_b32_e32 v26, v18
	v_mov_b32_e32 v27, v24
	v_mov_b32_e32 v38, v23
	v_mov_b32_e32 v39, v29
	v_pk_mul_f32 v[30:31], v[30:31], v[30:31]
	v_pk_fma_f32 v[4:5], v[44:45], v[74:75], v[4:5]
	v_mov_b32_e32 v32, v0
	v_mov_b32_e32 v33, v2
	v_mov_b32_e32 v36, v22
	v_mov_b32_e32 v37, v28
	v_pk_mul_f32 v[38:39], v[38:39], v[38:39]
	v_pk_fma_f32 v[26:27], v[26:27], v[26:27], v[30:31]
	v_mov_b32_e32 v34, v1
	v_mov_b32_e32 v35, v3
	v_mov_b32_e32 v40, v6
	v_mov_b32_e32 v41, v4
	v_pk_fma_f32 v[30:31], v[36:37], v[36:37], v[38:39]
	v_pk_fma_f32 v[26:27], v[32:33], v[32:33], v[26:27]
	v_mov_b32_e32 v42, v7
	v_mov_b32_e32 v43, v5
	v_pk_fma_f32 v[30:31], v[40:41], v[40:41], v[30:31]
	v_pk_fma_f32 v[26:27], v[34:35], v[34:35], v[26:27]
	v_pk_fma_f32 v[30:31], v[42:43], v[42:43], v[30:31]
	v_add_f32_e32 v26, v26, v27
	v_add_f32_e32 v26, v31, v26
	v_add_f32_e32 v26, v30, v26
	s_waitcnt lgkmcnt(0)
	s_nop 1
	v_add_f32_dpp v26, v26, v26 quad_perm:[1,0,3,2] row_mask:0xf bank_mask:0xf
	s_waitcnt lgkmcnt(0)
	s_nop 1
	v_add_f32_dpp v26, v26, v26 quad_perm:[2,3,0,1] row_mask:0xf bank_mask:0xf
	s_waitcnt lgkmcnt(0)
	s_nop 1
	v_add_f32_dpp v26, v26, v26 row_half_mirror row_mask:0xf bank_mask:0xf
	s_waitcnt lgkmcnt(0)
	s_nop 1
	v_add_f32_dpp v26, v26, v26 row_mirror row_mask:0xf bank_mask:0xf
	v_mov_b32_e32 v27, v26
	s_nop 1
	v_permlane16_swap_b32 v26, v27
	s_waitcnt lgkmcnt(0)
	v_add_f32_e32 v26, v26, v27
	ds_bpermute_b32 v27, v89, v26
	s_waitcnt lgkmcnt(0)
	v_add_f32_e32 v26, v26, v27
	v_fmamk_f32 v26, v26, 0x3a800000, v21
	v_mul_f32_e32 v27, 0x4b800000, v26
	v_cmp_gt_f32_e32 vcc, s2, v26
	s_nop 1
	v_cndmask_b32_e32 v26, v26, v27, vcc
	v_rsq_f32_e32 v26, v26
	s_nop 0
	v_mul_f32_e32 v27, 0x45800000, v26
	v_cndmask_b32_e32 v26, v26, v27, vcc
	v_pk_mul_f32 v[18:19], v[18:19], v[26:27] op_sel_hi:[1,0]
	v_pk_mul_f32 v[0:1], v[0:1], v[26:27] op_sel_hi:[1,0]
	v_pk_mul_f32 v[24:25], v[24:25], v[26:27] op_sel_hi:[1,0]
	v_pk_mul_f32 v[30:31], v[2:3], v[26:27] op_sel_hi:[1,0]
	v_pk_mul_f32 v[28:29], v[28:29], v[26:27] op_sel_hi:[1,0]
	v_pk_mul_f32 v[32:33], v[4:5], v[26:27] op_sel_hi:[1,0]
	v_pk_mul_f32 v[34:35], v[22:23], v[26:27] op_sel_hi:[1,0]
	v_pk_mul_f32 v[26:27], v[6:7], v[26:27] op_sel_hi:[1,0]
	s_waitcnt vmcnt(2)
	v_pk_mul_f32 v[2:3], v[52:53], v[0:1]
	v_pk_mul_f32 v[0:1], v[50:51], v[18:19]
	v_pk_mul_f32 v[6:7], v[48:49], v[30:31]
	v_pk_mul_f32 v[4:5], v[46:47], v[24:25]
	s_waitcnt vmcnt(0)
	v_pk_mul_f32 v[24:25], v[60:61], v[32:33]
	v_pk_mul_f32 v[22:23], v[58:59], v[28:29]
	v_pk_mul_f32 v[28:29], v[56:57], v[26:27]
	v_pk_mul_f32 v[26:27], v[54:55], v[34:35]
	global_store_dwordx4 v[16:17], v[0:3], off
	global_store_dwordx4 v[16:17], v[4:7], off offset:16
	global_store_dwordx4 v[16:17], v[22:25], off offset:2048
	global_store_dwordx4 v[16:17], v[26:29], off offset:2064
	v_lshl_add_u64 v[16:17], v[16:17], 0, s[10:11]
	s_andn2_b64 exec, exec, s[0:1]
	s_cbranch_execnz .LBB0_1574
